# speedup vs baseline: 1.0920x; 1.0009x over previous
.LBB1_32:
	s_or_b64 exec, exec, s[4:5]
	s_load_dwordx2 s[28:29], s[0:1], 0x18
	v_and_b32_e32 v240, 63, v0
	v_lshlrev_b32_e32 v240, 4, v240
	v_mov_b32_e32 v241, 0
	s_add_i32 s30, s13, -6
	s_lshl_b32 s27, s26, 1
	s_mov_b32 s33, 0
	s_waitcnt lgkmcnt(0)
	s_add_u32 s28, s28, 0x8000
	s_addc_u32 s29, s29, 0
	v_lshl_add_u64 v[240:241], s[28:29], 0, v[240:241]
.Lmy_k1dma:
	s_add_i32 s30, s30, 6
	s_add_i32 s32, s30, s27
	s_and_b32 s32, s32, 63
	s_lshl_b32 s32, s32, 10
	s_mov_b32 m0, s32
	v_lshl_add_u64 v[242:243], v[240:241], 0, s[32:33]
	global_load_lds_dwordx4 v[242:243], off
	s_cmp_lt_u32 s30, 58
	s_cbranch_scc1 .Lmy_k1dma
	v_lshl_add_u32 v2, v0, 2, 0
	s_movk_i32 s2, 0x290
	v_add_u32_e32 v2, 0x10000, v2
	v_cmp_gt_u32_e32 vcc, s2, v0
	s_waitcnt vmcnt(10)
	ds_write_b32 v2, v1
	s_and_saveexec_b64 s[2:3], vcc
	ds_write_b32 v2, v10 offset:1536
	s_or_b64 exec, exec, s[2:3]
	s_movk_i32 s2, 0x110
	v_cmp_gt_u32_e32 vcc, s2, v0
	s_and_saveexec_b64 s[2:3], vcc
	ds_write_b32 v2, v3 offset:3072
	s_or_b64 exec, exec, s[2:3]
	s_mulk_i32 s22, 0x180
	v_and_b32_e32 v1, 63, v0
	s_add_i32 s4, s22, 0
	s_add_i32 s4, s4, 0x11040
	v_cmp_gt_u32_e32 vcc, 32, v1
	s_and_saveexec_b64 s[2:3], vcc
	v_lshl_add_u32 v2, v9, 2, s4
	ds_write_b32 v2, v18
	s_or_b64 exec, exec, s[2:3]
	s_cmpk_gt_u32 s12, 0xfff
	s_waitcnt lgkmcnt(0)
	s_barrier
	s_cbranch_scc1 .LBB1_41
.LBB1_41:
	s_add_i32 s2, 0, 0x10200
	v_mov_b32_e32 v2, s2
	ds_read_b128 v[2:5], v2
	v_lshl_add_u32 v6, v8, 2, s4
	ds_read_b32 v56, v6 offset:256
	s_waitcnt lgkmcnt(0)
	v_lshrrev_b32_e32 v5, 5, v1
	v_lshlrev_b32_e32 v98, 4, v5
	v_add_u32_e32 v3, 0, v98
	v_add_u32_e32 v99, 0x10000, v3
	ds_read_b128 v[6:9], v99
	ds_read_b128 v[10:13], v99 offset:256
	v_mov_b32_e32 v19, s4
	ds_read_b128 v[14:17], v99 offset:32
	ds_read_b128 v[20:23], v99 offset:288
	s_add_i32 s2, 0, 0x10210
	v_mov_b32_e32 v57, s2
	s_waitcnt lgkmcnt(0)
	v_pk_fma_f32 v[44:45], v[18:19], v[6:7], v[10:11] op_sel_hi:[0,1,1]
	v_pk_fma_f32 v[46:47], v[18:19], v[8:9], v[12:13] op_sel_hi:[0,1,1]
	ds_read_b128 v[6:9], v99 offset:320
	ds_read_b128 v[10:13], v99 offset:64
	ds_read_b128 v[24:27], v99 offset:96
	ds_read_b128 v[28:31], v99 offset:352
	v_pk_fma_f32 v[40:41], v[18:19], v[14:15], v[20:21] op_sel_hi:[0,1,1]
	v_pk_fma_f32 v[42:43], v[18:19], v[16:17], v[22:23] op_sel_hi:[0,1,1]
	s_waitcnt lgkmcnt(0)
	v_pk_fma_f32 v[36:37], v[18:19], v[10:11], v[6:7] op_sel_hi:[0,1,1]
	v_pk_fma_f32 v[38:39], v[18:19], v[12:13], v[8:9] op_sel_hi:[0,1,1]
	v_pk_fma_f32 v[32:33], v[18:19], v[24:25], v[28:29] op_sel_hi:[0,1,1]
	v_pk_fma_f32 v[34:35], v[18:19], v[26:27], v[30:31] op_sel_hi:[0,1,1]
	ds_read_b128 v[6:9], v99 offset:384
	ds_read_b128 v[10:13], v99 offset:128
	ds_read_b128 v[14:17], v99 offset:160
	ds_read_b128 v[48:51], v99 offset:416
	ds_read_b128 v[20:23], v99 offset:192
	ds_read_b128 v[24:27], v99 offset:448
	s_waitcnt lgkmcnt(0)
	v_pk_fma_f32 v[28:29], v[18:19], v[10:11], v[6:7] op_sel_hi:[0,1,1]
	v_pk_fma_f32 v[30:31], v[18:19], v[12:13], v[8:9] op_sel_hi:[0,1,1]
	ds_read_b128 v[10:13], v99 offset:224
	ds_read_b128 v[52:55], v99 offset:480
	ds_read_b128 v[6:9], v57
	s_waitcnt lgkmcnt(0)
	v_lshl_add_u32 v7, v1, 2, s4
	v_fmac_f32_e32 v4, v18, v2
	v_pk_fma_f32 v[2:3], v[18:19], v[20:21], v[24:25] op_sel_hi:[0,1,1]
	v_pk_fma_f32 v[20:21], v[18:19], v[22:23], v[26:27] op_sel_hi:[0,1,1]
	ds_read_b32 v7, v7
	v_pk_fma_f32 v[22:23], v[18:19], v[10:11], v[52:53] op_sel_hi:[0,1,1]
	v_mbcnt_lo_u32_b32 v11, -1, 0
	v_mbcnt_hi_u32_b32 v52, -1, v11
	v_and_b32_e32 v11, 64, v52
	v_add_u32_e32 v53, 64, v11
	v_xor_b32_e32 v11, 1, v52
	v_cmp_lt_i32_e32 vcc, v11, v53
	v_max_f32_e32 v10, v56, v56
	s_waitcnt lgkmcnt(0)
	v_max_f32_e32 v7, v7, v7
	v_cndmask_b32_e32 v11, v52, v11, vcc
	v_max_f32_e32 v24, v7, v10
	v_lshlrev_b32_e32 v11, 2, v11
	s_add_i32 s2, 0, 0x10220
	ds_bpermute_b32 v25, v11, v24
	v_min_f32_e32 v7, v7, v10
	v_mov_b32_e32 v9, s2
	v_pk_fma_f32 v[26:27], v[18:19], v[12:13], v[54:55] op_sel_hi:[0,1,1]
	ds_bpermute_b32 v54, v11, v7
	ds_read_b128 v[10:13], v9
	s_waitcnt lgkmcnt(0)
	v_xor_b32_e32 v11, 2, v52
	v_cmp_lt_i32_e32 vcc, v11, v53
	v_fmac_f32_e32 v8, v18, v6
	v_max_f32_e32 v6, v25, v25
	v_cndmask_b32_e32 v11, v52, v11, vcc
	v_max_f32_e32 v6, v24, v6
	v_max_f32_e32 v9, v54, v54
	v_lshlrev_b32_e32 v11, 2, v11
	ds_bpermute_b32 v13, v11, v6
	v_min_f32_e32 v7, v7, v9
	ds_bpermute_b32 v9, v11, v7
	v_fmac_f32_e32 v12, v18, v10
	s_add_i32 s2, 0, 0x10230
	s_waitcnt lgkmcnt(0)
	v_max_f32_e32 v13, v13, v13
	v_max_f32_e32 v13, v6, v13
	v_max_f32_e32 v6, v9, v9
	v_xor_b32_e32 v9, 4, v52
	v_cmp_lt_i32_e32 vcc, v9, v53
	v_min_f32_e32 v55, v7, v6
	v_pk_fma_f32 v[6:7], v[18:19], v[14:15], v[48:49] op_sel_hi:[0,1,1]
	v_cndmask_b32_e32 v9, v52, v9, vcc
	v_lshlrev_b32_e32 v9, 2, v9
	ds_bpermute_b32 v54, v9, v13
	ds_bpermute_b32 v9, v9, v55
	v_mov_b32_e32 v11, s2
	s_movk_i32 s2, 0xc0
	v_pk_fma_f32 v[24:25], v[18:19], v[16:17], v[50:51] op_sel_hi:[0,1,1]
	s_waitcnt lgkmcnt(0)
	v_max_f32_e32 v14, v54, v54
	v_max_f32_e32 v13, v13, v14
	v_xor_b32_e32 v14, 8, v52
	v_cmp_lt_i32_e32 vcc, v14, v53
	v_max_f32_e32 v9, v9, v9
	v_min_f32_e32 v9, v55, v9
	v_cndmask_b32_e32 v14, v52, v14, vcc
	v_lshlrev_b32_e32 v14, 2, v14
	ds_bpermute_b32 v48, v14, v13
	ds_bpermute_b32 v49, v14, v9
	ds_read_b128 v[14:17], v11
	v_mad_u32_u24 v125, v5, s2, v19
	ds_read_b128 v[58:61], v125
	s_waitcnt lgkmcnt(0)
	v_max_f32_e32 v10, v48, v48
	v_max_f32_e32 v10, v13, v10
	v_xor_b32_e32 v13, 16, v52
	v_cmp_lt_i32_e32 vcc, v13, v53
	v_max_f32_e32 v11, v49, v49
	v_min_f32_e32 v9, v9, v11
	v_cndmask_b32_e32 v13, v52, v13, vcc
	v_lshlrev_b32_e32 v13, 2, v13
	ds_bpermute_b32 v15, v13, v10
	ds_bpermute_b32 v11, v13, v9
	v_fmac_f32_e32 v16, v18, v14
	ds_read_b128 v[86:89], v125 offset:16
	ds_read_b128 v[132:135], v125 offset:32
	s_waitcnt lgkmcnt(0)
	v_max_f32_e32 v13, v15, v15
	v_max_f32_e32 v10, v10, v13
	v_xor_b32_e32 v13, 32, v52
	v_cmp_lt_i32_e32 vcc, v13, v53
	v_max_f32_e32 v11, v11, v11
	v_min_f32_e32 v9, v9, v11
	v_cndmask_b32_e32 v13, v52, v13, vcc
	v_lshlrev_b32_e32 v13, 2, v13
	ds_bpermute_b32 v15, v13, v10
	ds_bpermute_b32 v11, v13, v9
	ds_read_b128 v[136:139], v125 offset:48
	ds_read_b128 v[148:151], v125 offset:64
	ds_read_b128 v[158:161], v125 offset:80
	ds_read_b128 v[180:183], v125 offset:96
	s_waitcnt lgkmcnt(0)
	v_max_f32_e32 v13, v15, v15
	v_max_f32_e32 v11, v11, v11
	v_max_f32_e32 v10, v10, v13
	v_min_f32_e32 v9, v9, v11
	v_mul_f32_e32 v11, v10, v4
	v_mul_f32_e32 v13, v9, v4
	v_max_f32_e32 v131, v11, v13
	v_mul_f32_e32 v11, v10, v8
	v_mul_f32_e32 v13, v9, v8
	v_max_f32_e32 v130, v11, v13
	v_mul_f32_e32 v11, v10, v12
	v_mul_f32_e32 v13, v9, v12
	v_mul_f32_e32 v10, v10, v16
	v_mul_f32_e32 v9, v9, v16
	v_max_f32_e32 v128, v10, v9
	v_max_f32_e32 v129, v11, v13
	s_waitcnt lgkmcnt(0)
	ds_read_b128 v[68:71], v125 offset:112
	ds_read_b128 v[92:95], v125 offset:128
	ds_read_b128 v[100:103], v125 offset:144
	ds_read_b128 v[104:107], v125 offset:160
	ds_read_b128 v[108:111], v125 offset:176
	v_mov_b32_e32 v140, v4
	v_mov_b32_e32 v141, v8
	v_mov_b32_e32 v142, v12
	v_mov_b32_e32 v143, v16
	v_mov_b32_e32 v144, v131
	v_mov_b32_e32 v145, v130
	v_mov_b32_e32 v146, v129
	v_mov_b32_e32 v147, v128
	v_mov_b32_e32 v152, 0
	v_mov_b32_e32 v153, 0
	v_mov_b32_e32 v154, 0
	v_mov_b32_e32 v155, 0
	v_mov_b32_e32 v164, 0
	v_mov_b32_e32 v165, 0
	v_mov_b32_e32 v166, 0
	v_mov_b32_e32 v167, 0
	v_pk_fma_f32 v[112:113], v[58:59], v[140:141], v[144:145] op_sel:[0,0,0] op_sel_hi:[0,1,1] neg_lo:[0,0,1] neg_hi:[0,0,1]
	v_pk_fma_f32 v[114:115], v[58:59], v[142:143], v[146:147] op_sel:[0,0,0] op_sel_hi:[0,1,1] neg_lo:[0,0,1] neg_hi:[0,0,1]
	v_exp_f32_e32 v112, v112
	v_exp_f32_e32 v113, v113
	v_exp_f32_e32 v114, v114
	v_exp_f32_e32 v115, v115
	v_pk_fma_f32 v[116:117], v[58:59], v[140:141], v[144:145] op_sel:[1,0,0] op_sel_hi:[1,1,1] neg_lo:[0,0,1] neg_hi:[0,0,1]
	v_pk_fma_f32 v[118:119], v[58:59], v[142:143], v[146:147] op_sel:[1,0,0] op_sel_hi:[1,1,1] neg_lo:[0,0,1] neg_hi:[0,0,1]
	v_exp_f32_e32 v116, v116
	v_exp_f32_e32 v117, v117
	v_exp_f32_e32 v118, v118
	v_exp_f32_e32 v119, v119
	v_pk_add_f32 v[152:153], v[152:153], v[112:113]
	v_pk_add_f32 v[154:155], v[154:155], v[114:115]
	v_pk_fma_f32 v[164:165], v[112:113], v[58:59], v[164:165] op_sel:[0,0,0] op_sel_hi:[1,0,1]
	v_pk_fma_f32 v[166:167], v[114:115], v[58:59], v[166:167] op_sel:[0,0,0] op_sel_hi:[1,0,1]
	v_pk_add_f32 v[152:153], v[152:153], v[116:117]
	v_pk_add_f32 v[154:155], v[154:155], v[118:119]
	v_pk_fma_f32 v[164:165], v[116:117], v[58:59], v[164:165] op_sel:[0,1,0] op_sel_hi:[1,1,1]
	v_pk_fma_f32 v[166:167], v[118:119], v[58:59], v[166:167] op_sel:[0,1,0] op_sel_hi:[1,1,1]
	v_pk_fma_f32 v[112:113], v[60:61], v[140:141], v[144:145] op_sel:[0,0,0] op_sel_hi:[0,1,1] neg_lo:[0,0,1] neg_hi:[0,0,1]
	v_pk_fma_f32 v[114:115], v[60:61], v[142:143], v[146:147] op_sel:[0,0,0] op_sel_hi:[0,1,1] neg_lo:[0,0,1] neg_hi:[0,0,1]
	v_exp_f32_e32 v112, v112
	v_exp_f32_e32 v113, v113
	v_exp_f32_e32 v114, v114
	v_exp_f32_e32 v115, v115
	v_pk_fma_f32 v[116:117], v[60:61], v[140:141], v[144:145] op_sel:[1,0,0] op_sel_hi:[1,1,1] neg_lo:[0,0,1] neg_hi:[0,0,1]
	v_pk_fma_f32 v[118:119], v[60:61], v[142:143], v[146:147] op_sel:[1,0,0] op_sel_hi:[1,1,1] neg_lo:[0,0,1] neg_hi:[0,0,1]
	v_exp_f32_e32 v116, v116
	v_exp_f32_e32 v117, v117
	v_exp_f32_e32 v118, v118
	v_exp_f32_e32 v119, v119
	v_pk_add_f32 v[152:153], v[152:153], v[112:113]
	v_pk_add_f32 v[154:155], v[154:155], v[114:115]
	v_pk_fma_f32 v[164:165], v[112:113], v[60:61], v[164:165] op_sel:[0,0,0] op_sel_hi:[1,0,1]
	v_pk_fma_f32 v[166:167], v[114:115], v[60:61], v[166:167] op_sel:[0,0,0] op_sel_hi:[1,0,1]
	v_pk_add_f32 v[152:153], v[152:153], v[116:117]
	v_pk_add_f32 v[154:155], v[154:155], v[118:119]
	v_pk_fma_f32 v[164:165], v[116:117], v[60:61], v[164:165] op_sel:[0,1,0] op_sel_hi:[1,1,1]
	v_pk_fma_f32 v[166:167], v[118:119], v[60:61], v[166:167] op_sel:[0,1,0] op_sel_hi:[1,1,1]
	v_pk_fma_f32 v[112:113], v[86:87], v[140:141], v[144:145] op_sel:[0,0,0] op_sel_hi:[0,1,1] neg_lo:[0,0,1] neg_hi:[0,0,1]
	v_pk_fma_f32 v[114:115], v[86:87], v[142:143], v[146:147] op_sel:[0,0,0] op_sel_hi:[0,1,1] neg_lo:[0,0,1] neg_hi:[0,0,1]
	v_exp_f32_e32 v112, v112
	v_exp_f32_e32 v113, v113
	v_exp_f32_e32 v114, v114
	v_exp_f32_e32 v115, v115
	v_pk_fma_f32 v[116:117], v[86:87], v[140:141], v[144:145] op_sel:[1,0,0] op_sel_hi:[1,1,1] neg_lo:[0,0,1] neg_hi:[0,0,1]
	v_pk_fma_f32 v[118:119], v[86:87], v[142:143], v[146:147] op_sel:[1,0,0] op_sel_hi:[1,1,1] neg_lo:[0,0,1] neg_hi:[0,0,1]
	v_exp_f32_e32 v116, v116
	v_exp_f32_e32 v117, v117
	v_exp_f32_e32 v118, v118
	v_exp_f32_e32 v119, v119
	v_pk_add_f32 v[152:153], v[152:153], v[112:113]
	v_pk_add_f32 v[154:155], v[154:155], v[114:115]
	v_pk_fma_f32 v[164:165], v[112:113], v[86:87], v[164:165] op_sel:[0,0,0] op_sel_hi:[1,0,1]
	v_pk_fma_f32 v[166:167], v[114:115], v[86:87], v[166:167] op_sel:[0,0,0] op_sel_hi:[1,0,1]
	v_pk_add_f32 v[152:153], v[152:153], v[116:117]
	v_pk_add_f32 v[154:155], v[154:155], v[118:119]
	v_pk_fma_f32 v[164:165], v[116:117], v[86:87], v[164:165] op_sel:[0,1,0] op_sel_hi:[1,1,1]
	v_pk_fma_f32 v[166:167], v[118:119], v[86:87], v[166:167] op_sel:[0,1,0] op_sel_hi:[1,1,1]
	v_pk_fma_f32 v[112:113], v[88:89], v[140:141], v[144:145] op_sel:[0,0,0] op_sel_hi:[0,1,1] neg_lo:[0,0,1] neg_hi:[0,0,1]
	v_pk_fma_f32 v[114:115], v[88:89], v[142:143], v[146:147] op_sel:[0,0,0] op_sel_hi:[0,1,1] neg_lo:[0,0,1] neg_hi:[0,0,1]
	v_exp_f32_e32 v112, v112
	v_exp_f32_e32 v113, v113
	v_exp_f32_e32 v114, v114
	v_exp_f32_e32 v115, v115
	v_pk_fma_f32 v[116:117], v[88:89], v[140:141], v[144:145] op_sel:[1,0,0] op_sel_hi:[1,1,1] neg_lo:[0,0,1] neg_hi:[0,0,1]
	v_pk_fma_f32 v[118:119], v[88:89], v[142:143], v[146:147] op_sel:[1,0,0] op_sel_hi:[1,1,1] neg_lo:[0,0,1] neg_hi:[0,0,1]
	v_exp_f32_e32 v116, v116
	v_exp_f32_e32 v117, v117
	v_exp_f32_e32 v118, v118
	v_exp_f32_e32 v119, v119
	v_pk_add_f32 v[152:153], v[152:153], v[112:113]
	v_pk_add_f32 v[154:155], v[154:155], v[114:115]
	v_pk_fma_f32 v[164:165], v[112:113], v[88:89], v[164:165] op_sel:[0,0,0] op_sel_hi:[1,0,1]
	v_pk_fma_f32 v[166:167], v[114:115], v[88:89], v[166:167] op_sel:[0,0,0] op_sel_hi:[1,0,1]
	v_pk_add_f32 v[152:153], v[152:153], v[116:117]
	v_pk_add_f32 v[154:155], v[154:155], v[118:119]
	v_pk_fma_f32 v[164:165], v[116:117], v[88:89], v[164:165] op_sel:[0,1,0] op_sel_hi:[1,1,1]
	v_pk_fma_f32 v[166:167], v[118:119], v[88:89], v[166:167] op_sel:[0,1,0] op_sel_hi:[1,1,1]
	v_pk_fma_f32 v[112:113], v[132:133], v[140:141], v[144:145] op_sel:[0,0,0] op_sel_hi:[0,1,1] neg_lo:[0,0,1] neg_hi:[0,0,1]
	v_pk_fma_f32 v[114:115], v[132:133], v[142:143], v[146:147] op_sel:[0,0,0] op_sel_hi:[0,1,1] neg_lo:[0,0,1] neg_hi:[0,0,1]
	v_exp_f32_e32 v112, v112
	v_exp_f32_e32 v113, v113
	v_exp_f32_e32 v114, v114
	v_exp_f32_e32 v115, v115
	v_pk_fma_f32 v[116:117], v[132:133], v[140:141], v[144:145] op_sel:[1,0,0] op_sel_hi:[1,1,1] neg_lo:[0,0,1] neg_hi:[0,0,1]
	v_pk_fma_f32 v[118:119], v[132:133], v[142:143], v[146:147] op_sel:[1,0,0] op_sel_hi:[1,1,1] neg_lo:[0,0,1] neg_hi:[0,0,1]
	v_exp_f32_e32 v116, v116
	v_exp_f32_e32 v117, v117
	v_exp_f32_e32 v118, v118
	v_exp_f32_e32 v119, v119
	v_pk_add_f32 v[152:153], v[152:153], v[112:113]
	v_pk_add_f32 v[154:155], v[154:155], v[114:115]
	v_pk_fma_f32 v[164:165], v[112:113], v[132:133], v[164:165] op_sel:[0,0,0] op_sel_hi:[1,0,1]
	v_pk_fma_f32 v[166:167], v[114:115], v[132:133], v[166:167] op_sel:[0,0,0] op_sel_hi:[1,0,1]
	v_pk_add_f32 v[152:153], v[152:153], v[116:117]
	v_pk_add_f32 v[154:155], v[154:155], v[118:119]
	v_pk_fma_f32 v[164:165], v[116:117], v[132:133], v[164:165] op_sel:[0,1,0] op_sel_hi:[1,1,1]
	v_pk_fma_f32 v[166:167], v[118:119], v[132:133], v[166:167] op_sel:[0,1,0] op_sel_hi:[1,1,1]
	v_pk_fma_f32 v[112:113], v[134:135], v[140:141], v[144:145] op_sel:[0,0,0] op_sel_hi:[0,1,1] neg_lo:[0,0,1] neg_hi:[0,0,1]
	v_pk_fma_f32 v[114:115], v[134:135], v[142:143], v[146:147] op_sel:[0,0,0] op_sel_hi:[0,1,1] neg_lo:[0,0,1] neg_hi:[0,0,1]
	v_exp_f32_e32 v112, v112
	v_exp_f32_e32 v113, v113
	v_exp_f32_e32 v114, v114
	v_exp_f32_e32 v115, v115
	v_pk_fma_f32 v[116:117], v[134:135], v[140:141], v[144:145] op_sel:[1,0,0] op_sel_hi:[1,1,1] neg_lo:[0,0,1] neg_hi:[0,0,1]
	v_pk_fma_f32 v[118:119], v[134:135], v[142:143], v[146:147] op_sel:[1,0,0] op_sel_hi:[1,1,1] neg_lo:[0,0,1] neg_hi:[0,0,1]
	v_exp_f32_e32 v116, v116
	v_exp_f32_e32 v117, v117
	v_exp_f32_e32 v118, v118
	v_exp_f32_e32 v119, v119
	v_pk_add_f32 v[152:153], v[152:153], v[112:113]
	v_pk_add_f32 v[154:155], v[154:155], v[114:115]
	v_pk_fma_f32 v[164:165], v[112:113], v[134:135], v[164:165] op_sel:[0,0,0] op_sel_hi:[1,0,1]
	v_pk_fma_f32 v[166:167], v[114:115], v[134:135], v[166:167] op_sel:[0,0,0] op_sel_hi:[1,0,1]
	v_pk_add_f32 v[152:153], v[152:153], v[116:117]
	v_pk_add_f32 v[154:155], v[154:155], v[118:119]
	v_pk_fma_f32 v[164:165], v[116:117], v[134:135], v[164:165] op_sel:[0,1,0] op_sel_hi:[1,1,1]
	v_pk_fma_f32 v[166:167], v[118:119], v[134:135], v[166:167] op_sel:[0,1,0] op_sel_hi:[1,1,1]
	v_pk_fma_f32 v[112:113], v[136:137], v[140:141], v[144:145] op_sel:[0,0,0] op_sel_hi:[0,1,1] neg_lo:[0,0,1] neg_hi:[0,0,1]
	v_pk_fma_f32 v[114:115], v[136:137], v[142:143], v[146:147] op_sel:[0,0,0] op_sel_hi:[0,1,1] neg_lo:[0,0,1] neg_hi:[0,0,1]
	v_exp_f32_e32 v112, v112
	v_exp_f32_e32 v113, v113
	v_exp_f32_e32 v114, v114
	v_exp_f32_e32 v115, v115
	v_pk_fma_f32 v[116:117], v[136:137], v[140:141], v[144:145] op_sel:[1,0,0] op_sel_hi:[1,1,1] neg_lo:[0,0,1] neg_hi:[0,0,1]
	v_pk_fma_f32 v[118:119], v[136:137], v[142:143], v[146:147] op_sel:[1,0,0] op_sel_hi:[1,1,1] neg_lo:[0,0,1] neg_hi:[0,0,1]
	v_exp_f32_e32 v116, v116
	v_exp_f32_e32 v117, v117
	v_exp_f32_e32 v118, v118
	v_exp_f32_e32 v119, v119
	v_pk_add_f32 v[152:153], v[152:153], v[112:113]
	v_pk_add_f32 v[154:155], v[154:155], v[114:115]
	v_pk_fma_f32 v[164:165], v[112:113], v[136:137], v[164:165] op_sel:[0,0,0] op_sel_hi:[1,0,1]
	v_pk_fma_f32 v[166:167], v[114:115], v[136:137], v[166:167] op_sel:[0,0,0] op_sel_hi:[1,0,1]
	v_pk_add_f32 v[152:153], v[152:153], v[116:117]
	v_pk_add_f32 v[154:155], v[154:155], v[118:119]
	v_pk_fma_f32 v[164:165], v[116:117], v[136:137], v[164:165] op_sel:[0,1,0] op_sel_hi:[1,1,1]
	v_pk_fma_f32 v[166:167], v[118:119], v[136:137], v[166:167] op_sel:[0,1,0] op_sel_hi:[1,1,1]
	v_pk_fma_f32 v[112:113], v[138:139], v[140:141], v[144:145] op_sel:[0,0,0] op_sel_hi:[0,1,1] neg_lo:[0,0,1] neg_hi:[0,0,1]
	v_pk_fma_f32 v[114:115], v[138:139], v[142:143], v[146:147] op_sel:[0,0,0] op_sel_hi:[0,1,1] neg_lo:[0,0,1] neg_hi:[0,0,1]
	v_exp_f32_e32 v112, v112
	v_exp_f32_e32 v113, v113
	v_exp_f32_e32 v114, v114
	v_exp_f32_e32 v115, v115
	v_pk_fma_f32 v[116:117], v[138:139], v[140:141], v[144:145] op_sel:[1,0,0] op_sel_hi:[1,1,1] neg_lo:[0,0,1] neg_hi:[0,0,1]
	v_pk_fma_f32 v[118:119], v[138:139], v[142:143], v[146:147] op_sel:[1,0,0] op_sel_hi:[1,1,1] neg_lo:[0,0,1] neg_hi:[0,0,1]
	v_exp_f32_e32 v116, v116
	v_exp_f32_e32 v117, v117
	v_exp_f32_e32 v118, v118
	v_exp_f32_e32 v119, v119
	v_pk_add_f32 v[152:153], v[152:153], v[112:113]
	v_pk_add_f32 v[154:155], v[154:155], v[114:115]
	v_pk_fma_f32 v[164:165], v[112:113], v[138:139], v[164:165] op_sel:[0,0,0] op_sel_hi:[1,0,1]
	v_pk_fma_f32 v[166:167], v[114:115], v[138:139], v[166:167] op_sel:[0,0,0] op_sel_hi:[1,0,1]
	v_pk_add_f32 v[152:153], v[152:153], v[116:117]
	v_pk_add_f32 v[154:155], v[154:155], v[118:119]
	v_pk_fma_f32 v[164:165], v[116:117], v[138:139], v[164:165] op_sel:[0,1,0] op_sel_hi:[1,1,1]
	v_pk_fma_f32 v[166:167], v[118:119], v[138:139], v[166:167] op_sel:[0,1,0] op_sel_hi:[1,1,1]
	v_pk_fma_f32 v[112:113], v[148:149], v[140:141], v[144:145] op_sel:[0,0,0] op_sel_hi:[0,1,1] neg_lo:[0,0,1] neg_hi:[0,0,1]
	v_pk_fma_f32 v[114:115], v[148:149], v[142:143], v[146:147] op_sel:[0,0,0] op_sel_hi:[0,1,1] neg_lo:[0,0,1] neg_hi:[0,0,1]
	v_exp_f32_e32 v112, v112
	v_exp_f32_e32 v113, v113
	v_exp_f32_e32 v114, v114
	v_exp_f32_e32 v115, v115
	v_pk_fma_f32 v[116:117], v[148:149], v[140:141], v[144:145] op_sel:[1,0,0] op_sel_hi:[1,1,1] neg_lo:[0,0,1] neg_hi:[0,0,1]
	v_pk_fma_f32 v[118:119], v[148:149], v[142:143], v[146:147] op_sel:[1,0,0] op_sel_hi:[1,1,1] neg_lo:[0,0,1] neg_hi:[0,0,1]
	v_exp_f32_e32 v116, v116
	v_exp_f32_e32 v117, v117
	v_exp_f32_e32 v118, v118
	v_exp_f32_e32 v119, v119
	v_pk_add_f32 v[152:153], v[152:153], v[112:113]
	v_pk_add_f32 v[154:155], v[154:155], v[114:115]
	v_pk_fma_f32 v[164:165], v[112:113], v[148:149], v[164:165] op_sel:[0,0,0] op_sel_hi:[1,0,1]
	v_pk_fma_f32 v[166:167], v[114:115], v[148:149], v[166:167] op_sel:[0,0,0] op_sel_hi:[1,0,1]
	v_pk_add_f32 v[152:153], v[152:153], v[116:117]
	v_pk_add_f32 v[154:155], v[154:155], v[118:119]
	v_pk_fma_f32 v[164:165], v[116:117], v[148:149], v[164:165] op_sel:[0,1,0] op_sel_hi:[1,1,1]
	v_pk_fma_f32 v[166:167], v[118:119], v[148:149], v[166:167] op_sel:[0,1,0] op_sel_hi:[1,1,1]
	v_pk_fma_f32 v[112:113], v[150:151], v[140:141], v[144:145] op_sel:[0,0,0] op_sel_hi:[0,1,1] neg_lo:[0,0,1] neg_hi:[0,0,1]
	v_pk_fma_f32 v[114:115], v[150:151], v[142:143], v[146:147] op_sel:[0,0,0] op_sel_hi:[0,1,1] neg_lo:[0,0,1] neg_hi:[0,0,1]
	v_exp_f32_e32 v112, v112
	v_exp_f32_e32 v113, v113
	v_exp_f32_e32 v114, v114
	v_exp_f32_e32 v115, v115
	v_pk_fma_f32 v[116:117], v[150:151], v[140:141], v[144:145] op_sel:[1,0,0] op_sel_hi:[1,1,1] neg_lo:[0,0,1] neg_hi:[0,0,1]
	v_pk_fma_f32 v[118:119], v[150:151], v[142:143], v[146:147] op_sel:[1,0,0] op_sel_hi:[1,1,1] neg_lo:[0,0,1] neg_hi:[0,0,1]
	v_exp_f32_e32 v116, v116
	v_exp_f32_e32 v117, v117
	v_exp_f32_e32 v118, v118
	v_exp_f32_e32 v119, v119
	v_pk_add_f32 v[152:153], v[152:153], v[112:113]
	v_pk_add_f32 v[154:155], v[154:155], v[114:115]
	v_pk_fma_f32 v[164:165], v[112:113], v[150:151], v[164:165] op_sel:[0,0,0] op_sel_hi:[1,0,1]
	v_pk_fma_f32 v[166:167], v[114:115], v[150:151], v[166:167] op_sel:[0,0,0] op_sel_hi:[1,0,1]
	v_pk_add_f32 v[152:153], v[152:153], v[116:117]
	v_pk_add_f32 v[154:155], v[154:155], v[118:119]
	v_pk_fma_f32 v[164:165], v[116:117], v[150:151], v[164:165] op_sel:[0,1,0] op_sel_hi:[1,1,1]
	v_pk_fma_f32 v[166:167], v[118:119], v[150:151], v[166:167] op_sel:[0,1,0] op_sel_hi:[1,1,1]
	v_pk_fma_f32 v[112:113], v[158:159], v[140:141], v[144:145] op_sel:[0,0,0] op_sel_hi:[0,1,1] neg_lo:[0,0,1] neg_hi:[0,0,1]
	v_pk_fma_f32 v[114:115], v[158:159], v[142:143], v[146:147] op_sel:[0,0,0] op_sel_hi:[0,1,1] neg_lo:[0,0,1] neg_hi:[0,0,1]
	v_exp_f32_e32 v112, v112
	v_exp_f32_e32 v113, v113
	v_exp_f32_e32 v114, v114
	v_exp_f32_e32 v115, v115
	v_pk_fma_f32 v[116:117], v[158:159], v[140:141], v[144:145] op_sel:[1,0,0] op_sel_hi:[1,1,1] neg_lo:[0,0,1] neg_hi:[0,0,1]
	v_pk_fma_f32 v[118:119], v[158:159], v[142:143], v[146:147] op_sel:[1,0,0] op_sel_hi:[1,1,1] neg_lo:[0,0,1] neg_hi:[0,0,1]
	v_exp_f32_e32 v116, v116
	v_exp_f32_e32 v117, v117
	v_exp_f32_e32 v118, v118
	v_exp_f32_e32 v119, v119
	v_pk_add_f32 v[152:153], v[152:153], v[112:113]
	v_pk_add_f32 v[154:155], v[154:155], v[114:115]
	v_pk_fma_f32 v[164:165], v[112:113], v[158:159], v[164:165] op_sel:[0,0,0] op_sel_hi:[1,0,1]
	v_pk_fma_f32 v[166:167], v[114:115], v[158:159], v[166:167] op_sel:[0,0,0] op_sel_hi:[1,0,1]
	v_pk_add_f32 v[152:153], v[152:153], v[116:117]
	v_pk_add_f32 v[154:155], v[154:155], v[118:119]
	v_pk_fma_f32 v[164:165], v[116:117], v[158:159], v[164:165] op_sel:[0,1,0] op_sel_hi:[1,1,1]
	v_pk_fma_f32 v[166:167], v[118:119], v[158:159], v[166:167] op_sel:[0,1,0] op_sel_hi:[1,1,1]
	v_pk_fma_f32 v[112:113], v[160:161], v[140:141], v[144:145] op_sel:[0,0,0] op_sel_hi:[0,1,1] neg_lo:[0,0,1] neg_hi:[0,0,1]
	v_pk_fma_f32 v[114:115], v[160:161], v[142:143], v[146:147] op_sel:[0,0,0] op_sel_hi:[0,1,1] neg_lo:[0,0,1] neg_hi:[0,0,1]
	v_exp_f32_e32 v112, v112
	v_exp_f32_e32 v113, v113
	v_exp_f32_e32 v114, v114
	v_exp_f32_e32 v115, v115
	v_pk_fma_f32 v[116:117], v[160:161], v[140:141], v[144:145] op_sel:[1,0,0] op_sel_hi:[1,1,1] neg_lo:[0,0,1] neg_hi:[0,0,1]
	v_pk_fma_f32 v[118:119], v[160:161], v[142:143], v[146:147] op_sel:[1,0,0] op_sel_hi:[1,1,1] neg_lo:[0,0,1] neg_hi:[0,0,1]
	v_exp_f32_e32 v116, v116
	v_exp_f32_e32 v117, v117
	v_exp_f32_e32 v118, v118
	v_exp_f32_e32 v119, v119
	v_pk_add_f32 v[152:153], v[152:153], v[112:113]
	v_pk_add_f32 v[154:155], v[154:155], v[114:115]
	v_pk_fma_f32 v[164:165], v[112:113], v[160:161], v[164:165] op_sel:[0,0,0] op_sel_hi:[1,0,1]
	v_pk_fma_f32 v[166:167], v[114:115], v[160:161], v[166:167] op_sel:[0,0,0] op_sel_hi:[1,0,1]
	v_pk_add_f32 v[152:153], v[152:153], v[116:117]
	v_pk_add_f32 v[154:155], v[154:155], v[118:119]
	v_pk_fma_f32 v[164:165], v[116:117], v[160:161], v[164:165] op_sel:[0,1,0] op_sel_hi:[1,1,1]
	v_pk_fma_f32 v[166:167], v[118:119], v[160:161], v[166:167] op_sel:[0,1,0] op_sel_hi:[1,1,1]
	v_pk_fma_f32 v[112:113], v[180:181], v[140:141], v[144:145] op_sel:[0,0,0] op_sel_hi:[0,1,1] neg_lo:[0,0,1] neg_hi:[0,0,1]
	v_pk_fma_f32 v[114:115], v[180:181], v[142:143], v[146:147] op_sel:[0,0,0] op_sel_hi:[0,1,1] neg_lo:[0,0,1] neg_hi:[0,0,1]
	v_exp_f32_e32 v112, v112
	v_exp_f32_e32 v113, v113
	v_exp_f32_e32 v114, v114
	v_exp_f32_e32 v115, v115
	v_pk_fma_f32 v[116:117], v[180:181], v[140:141], v[144:145] op_sel:[1,0,0] op_sel_hi:[1,1,1] neg_lo:[0,0,1] neg_hi:[0,0,1]
	v_pk_fma_f32 v[118:119], v[180:181], v[142:143], v[146:147] op_sel:[1,0,0] op_sel_hi:[1,1,1] neg_lo:[0,0,1] neg_hi:[0,0,1]
	v_exp_f32_e32 v116, v116
	v_exp_f32_e32 v117, v117
	v_exp_f32_e32 v118, v118
	v_exp_f32_e32 v119, v119
	v_pk_add_f32 v[152:153], v[152:153], v[112:113]
	v_pk_add_f32 v[154:155], v[154:155], v[114:115]
	v_pk_fma_f32 v[164:165], v[112:113], v[180:181], v[164:165] op_sel:[0,0,0] op_sel_hi:[1,0,1]
	v_pk_fma_f32 v[166:167], v[114:115], v[180:181], v[166:167] op_sel:[0,0,0] op_sel_hi:[1,0,1]
	v_pk_add_f32 v[152:153], v[152:153], v[116:117]
	v_pk_add_f32 v[154:155], v[154:155], v[118:119]
	v_pk_fma_f32 v[164:165], v[116:117], v[180:181], v[164:165] op_sel:[0,1,0] op_sel_hi:[1,1,1]
	v_pk_fma_f32 v[166:167], v[118:119], v[180:181], v[166:167] op_sel:[0,1,0] op_sel_hi:[1,1,1]
	v_pk_fma_f32 v[112:113], v[182:183], v[140:141], v[144:145] op_sel:[0,0,0] op_sel_hi:[0,1,1] neg_lo:[0,0,1] neg_hi:[0,0,1]
	v_pk_fma_f32 v[114:115], v[182:183], v[142:143], v[146:147] op_sel:[0,0,0] op_sel_hi:[0,1,1] neg_lo:[0,0,1] neg_hi:[0,0,1]
	v_exp_f32_e32 v112, v112
	v_exp_f32_e32 v113, v113
	v_exp_f32_e32 v114, v114
	v_exp_f32_e32 v115, v115
	v_pk_fma_f32 v[116:117], v[182:183], v[140:141], v[144:145] op_sel:[1,0,0] op_sel_hi:[1,1,1] neg_lo:[0,0,1] neg_hi:[0,0,1]
	v_pk_fma_f32 v[118:119], v[182:183], v[142:143], v[146:147] op_sel:[1,0,0] op_sel_hi:[1,1,1] neg_lo:[0,0,1] neg_hi:[0,0,1]
	v_exp_f32_e32 v116, v116
	v_exp_f32_e32 v117, v117
	v_exp_f32_e32 v118, v118
	v_exp_f32_e32 v119, v119
	v_pk_add_f32 v[152:153], v[152:153], v[112:113]
	v_pk_add_f32 v[154:155], v[154:155], v[114:115]
	v_pk_fma_f32 v[164:165], v[112:113], v[182:183], v[164:165] op_sel:[0,0,0] op_sel_hi:[1,0,1]
	v_pk_fma_f32 v[166:167], v[114:115], v[182:183], v[166:167] op_sel:[0,0,0] op_sel_hi:[1,0,1]
	v_pk_add_f32 v[152:153], v[152:153], v[116:117]
	v_pk_add_f32 v[154:155], v[154:155], v[118:119]
	v_pk_fma_f32 v[164:165], v[116:117], v[182:183], v[164:165] op_sel:[0,1,0] op_sel_hi:[1,1,1]
	v_pk_fma_f32 v[166:167], v[118:119], v[182:183], v[166:167] op_sel:[0,1,0] op_sel_hi:[1,1,1]
	s_waitcnt lgkmcnt(0)
	v_pk_fma_f32 v[112:113], v[68:69], v[140:141], v[144:145] op_sel:[0,0,0] op_sel_hi:[0,1,1] neg_lo:[0,0,1] neg_hi:[0,0,1]
	v_pk_fma_f32 v[114:115], v[68:69], v[142:143], v[146:147] op_sel:[0,0,0] op_sel_hi:[0,1,1] neg_lo:[0,0,1] neg_hi:[0,0,1]
	v_exp_f32_e32 v112, v112
	v_exp_f32_e32 v113, v113
	v_exp_f32_e32 v114, v114
	v_exp_f32_e32 v115, v115
	v_pk_fma_f32 v[116:117], v[68:69], v[140:141], v[144:145] op_sel:[1,0,0] op_sel_hi:[1,1,1] neg_lo:[0,0,1] neg_hi:[0,0,1]
	v_pk_fma_f32 v[118:119], v[68:69], v[142:143], v[146:147] op_sel:[1,0,0] op_sel_hi:[1,1,1] neg_lo:[0,0,1] neg_hi:[0,0,1]
	v_exp_f32_e32 v116, v116
	v_exp_f32_e32 v117, v117
	v_exp_f32_e32 v118, v118
	v_exp_f32_e32 v119, v119
	v_pk_add_f32 v[152:153], v[152:153], v[112:113]
	v_pk_add_f32 v[154:155], v[154:155], v[114:115]
	v_pk_fma_f32 v[164:165], v[112:113], v[68:69], v[164:165] op_sel:[0,0,0] op_sel_hi:[1,0,1]
	v_pk_fma_f32 v[166:167], v[114:115], v[68:69], v[166:167] op_sel:[0,0,0] op_sel_hi:[1,0,1]
	v_pk_add_f32 v[152:153], v[152:153], v[116:117]
	v_pk_add_f32 v[154:155], v[154:155], v[118:119]
	v_pk_fma_f32 v[164:165], v[116:117], v[68:69], v[164:165] op_sel:[0,1,0] op_sel_hi:[1,1,1]
	v_pk_fma_f32 v[166:167], v[118:119], v[68:69], v[166:167] op_sel:[0,1,0] op_sel_hi:[1,1,1]
	v_pk_fma_f32 v[112:113], v[70:71], v[140:141], v[144:145] op_sel:[0,0,0] op_sel_hi:[0,1,1] neg_lo:[0,0,1] neg_hi:[0,0,1]
	v_pk_fma_f32 v[114:115], v[70:71], v[142:143], v[146:147] op_sel:[0,0,0] op_sel_hi:[0,1,1] neg_lo:[0,0,1] neg_hi:[0,0,1]
	v_exp_f32_e32 v112, v112
	v_exp_f32_e32 v113, v113
	v_exp_f32_e32 v114, v114
	v_exp_f32_e32 v115, v115
	v_pk_fma_f32 v[116:117], v[70:71], v[140:141], v[144:145] op_sel:[1,0,0] op_sel_hi:[1,1,1] neg_lo:[0,0,1] neg_hi:[0,0,1]
	v_pk_fma_f32 v[118:119], v[70:71], v[142:143], v[146:147] op_sel:[1,0,0] op_sel_hi:[1,1,1] neg_lo:[0,0,1] neg_hi:[0,0,1]
	v_exp_f32_e32 v116, v116
	v_exp_f32_e32 v117, v117
	v_exp_f32_e32 v118, v118
	v_exp_f32_e32 v119, v119
	v_pk_add_f32 v[152:153], v[152:153], v[112:113]
	v_pk_add_f32 v[154:155], v[154:155], v[114:115]
	v_pk_fma_f32 v[164:165], v[112:113], v[70:71], v[164:165] op_sel:[0,0,0] op_sel_hi:[1,0,1]
	v_pk_fma_f32 v[166:167], v[114:115], v[70:71], v[166:167] op_sel:[0,0,0] op_sel_hi:[1,0,1]
	v_pk_add_f32 v[152:153], v[152:153], v[116:117]
	v_pk_add_f32 v[154:155], v[154:155], v[118:119]
	v_pk_fma_f32 v[164:165], v[116:117], v[70:71], v[164:165] op_sel:[0,1,0] op_sel_hi:[1,1,1]
	v_pk_fma_f32 v[166:167], v[118:119], v[70:71], v[166:167] op_sel:[0,1,0] op_sel_hi:[1,1,1]
	v_pk_fma_f32 v[112:113], v[92:93], v[140:141], v[144:145] op_sel:[0,0,0] op_sel_hi:[0,1,1] neg_lo:[0,0,1] neg_hi:[0,0,1]
	v_pk_fma_f32 v[114:115], v[92:93], v[142:143], v[146:147] op_sel:[0,0,0] op_sel_hi:[0,1,1] neg_lo:[0,0,1] neg_hi:[0,0,1]
	v_exp_f32_e32 v112, v112
	v_exp_f32_e32 v113, v113
	v_exp_f32_e32 v114, v114
	v_exp_f32_e32 v115, v115
	v_pk_fma_f32 v[116:117], v[92:93], v[140:141], v[144:145] op_sel:[1,0,0] op_sel_hi:[1,1,1] neg_lo:[0,0,1] neg_hi:[0,0,1]
	v_pk_fma_f32 v[118:119], v[92:93], v[142:143], v[146:147] op_sel:[1,0,0] op_sel_hi:[1,1,1] neg_lo:[0,0,1] neg_hi:[0,0,1]
	v_exp_f32_e32 v116, v116
	v_exp_f32_e32 v117, v117
	v_exp_f32_e32 v118, v118
	v_exp_f32_e32 v119, v119
	v_pk_add_f32 v[152:153], v[152:153], v[112:113]
	v_pk_add_f32 v[154:155], v[154:155], v[114:115]
	v_pk_fma_f32 v[164:165], v[112:113], v[92:93], v[164:165] op_sel:[0,0,0] op_sel_hi:[1,0,1]
	v_pk_fma_f32 v[166:167], v[114:115], v[92:93], v[166:167] op_sel:[0,0,0] op_sel_hi:[1,0,1]
	v_pk_add_f32 v[152:153], v[152:153], v[116:117]
	v_pk_add_f32 v[154:155], v[154:155], v[118:119]
	v_pk_fma_f32 v[164:165], v[116:117], v[92:93], v[164:165] op_sel:[0,1,0] op_sel_hi:[1,1,1]
	v_pk_fma_f32 v[166:167], v[118:119], v[92:93], v[166:167] op_sel:[0,1,0] op_sel_hi:[1,1,1]
	v_pk_fma_f32 v[112:113], v[94:95], v[140:141], v[144:145] op_sel:[0,0,0] op_sel_hi:[0,1,1] neg_lo:[0,0,1] neg_hi:[0,0,1]
	v_pk_fma_f32 v[114:115], v[94:95], v[142:143], v[146:147] op_sel:[0,0,0] op_sel_hi:[0,1,1] neg_lo:[0,0,1] neg_hi:[0,0,1]
	v_exp_f32_e32 v112, v112
	v_exp_f32_e32 v113, v113
	v_exp_f32_e32 v114, v114
	v_exp_f32_e32 v115, v115
	v_pk_fma_f32 v[116:117], v[94:95], v[140:141], v[144:145] op_sel:[1,0,0] op_sel_hi:[1,1,1] neg_lo:[0,0,1] neg_hi:[0,0,1]
	v_pk_fma_f32 v[118:119], v[94:95], v[142:143], v[146:147] op_sel:[1,0,0] op_sel_hi:[1,1,1] neg_lo:[0,0,1] neg_hi:[0,0,1]
	v_exp_f32_e32 v116, v116
	v_exp_f32_e32 v117, v117
	v_exp_f32_e32 v118, v118
	v_exp_f32_e32 v119, v119
	v_pk_add_f32 v[152:153], v[152:153], v[112:113]
	v_pk_add_f32 v[154:155], v[154:155], v[114:115]
	v_pk_fma_f32 v[164:165], v[112:113], v[94:95], v[164:165] op_sel:[0,0,0] op_sel_hi:[1,0,1]
	v_pk_fma_f32 v[166:167], v[114:115], v[94:95], v[166:167] op_sel:[0,0,0] op_sel_hi:[1,0,1]
	v_pk_add_f32 v[152:153], v[152:153], v[116:117]
	v_pk_add_f32 v[154:155], v[154:155], v[118:119]
	v_pk_fma_f32 v[164:165], v[116:117], v[94:95], v[164:165] op_sel:[0,1,0] op_sel_hi:[1,1,1]
	v_pk_fma_f32 v[166:167], v[118:119], v[94:95], v[166:167] op_sel:[0,1,0] op_sel_hi:[1,1,1]
	v_pk_fma_f32 v[112:113], v[100:101], v[140:141], v[144:145] op_sel:[0,0,0] op_sel_hi:[0,1,1] neg_lo:[0,0,1] neg_hi:[0,0,1]
	v_pk_fma_f32 v[114:115], v[100:101], v[142:143], v[146:147] op_sel:[0,0,0] op_sel_hi:[0,1,1] neg_lo:[0,0,1] neg_hi:[0,0,1]
	v_exp_f32_e32 v112, v112
	v_exp_f32_e32 v113, v113
	v_exp_f32_e32 v114, v114
	v_exp_f32_e32 v115, v115
	v_pk_fma_f32 v[116:117], v[100:101], v[140:141], v[144:145] op_sel:[1,0,0] op_sel_hi:[1,1,1] neg_lo:[0,0,1] neg_hi:[0,0,1]
	v_pk_fma_f32 v[118:119], v[100:101], v[142:143], v[146:147] op_sel:[1,0,0] op_sel_hi:[1,1,1] neg_lo:[0,0,1] neg_hi:[0,0,1]
	v_exp_f32_e32 v116, v116
	v_exp_f32_e32 v117, v117
	v_exp_f32_e32 v118, v118
	v_exp_f32_e32 v119, v119
	v_pk_add_f32 v[152:153], v[152:153], v[112:113]
	v_pk_add_f32 v[154:155], v[154:155], v[114:115]
	v_pk_fma_f32 v[164:165], v[112:113], v[100:101], v[164:165] op_sel:[0,0,0] op_sel_hi:[1,0,1]
	v_pk_fma_f32 v[166:167], v[114:115], v[100:101], v[166:167] op_sel:[0,0,0] op_sel_hi:[1,0,1]
	v_pk_add_f32 v[152:153], v[152:153], v[116:117]
	v_pk_add_f32 v[154:155], v[154:155], v[118:119]
	v_pk_fma_f32 v[164:165], v[116:117], v[100:101], v[164:165] op_sel:[0,1,0] op_sel_hi:[1,1,1]
	v_pk_fma_f32 v[166:167], v[118:119], v[100:101], v[166:167] op_sel:[0,1,0] op_sel_hi:[1,1,1]
	v_pk_fma_f32 v[112:113], v[102:103], v[140:141], v[144:145] op_sel:[0,0,0] op_sel_hi:[0,1,1] neg_lo:[0,0,1] neg_hi:[0,0,1]
	v_pk_fma_f32 v[114:115], v[102:103], v[142:143], v[146:147] op_sel:[0,0,0] op_sel_hi:[0,1,1] neg_lo:[0,0,1] neg_hi:[0,0,1]
	v_exp_f32_e32 v112, v112
	v_exp_f32_e32 v113, v113
	v_exp_f32_e32 v114, v114
	v_exp_f32_e32 v115, v115
	v_pk_fma_f32 v[116:117], v[102:103], v[140:141], v[144:145] op_sel:[1,0,0] op_sel_hi:[1,1,1] neg_lo:[0,0,1] neg_hi:[0,0,1]
	v_pk_fma_f32 v[118:119], v[102:103], v[142:143], v[146:147] op_sel:[1,0,0] op_sel_hi:[1,1,1] neg_lo:[0,0,1] neg_hi:[0,0,1]
	v_exp_f32_e32 v116, v116
	v_exp_f32_e32 v117, v117
	v_exp_f32_e32 v118, v118
	v_exp_f32_e32 v119, v119
	v_pk_add_f32 v[152:153], v[152:153], v[112:113]
	v_pk_add_f32 v[154:155], v[154:155], v[114:115]
	v_pk_fma_f32 v[164:165], v[112:113], v[102:103], v[164:165] op_sel:[0,0,0] op_sel_hi:[1,0,1]
	v_pk_fma_f32 v[166:167], v[114:115], v[102:103], v[166:167] op_sel:[0,0,0] op_sel_hi:[1,0,1]
	v_pk_add_f32 v[152:153], v[152:153], v[116:117]
	v_pk_add_f32 v[154:155], v[154:155], v[118:119]
	v_pk_fma_f32 v[164:165], v[116:117], v[102:103], v[164:165] op_sel:[0,1,0] op_sel_hi:[1,1,1]
	v_pk_fma_f32 v[166:167], v[118:119], v[102:103], v[166:167] op_sel:[0,1,0] op_sel_hi:[1,1,1]
	v_pk_fma_f32 v[112:113], v[104:105], v[140:141], v[144:145] op_sel:[0,0,0] op_sel_hi:[0,1,1] neg_lo:[0,0,1] neg_hi:[0,0,1]
	v_pk_fma_f32 v[114:115], v[104:105], v[142:143], v[146:147] op_sel:[0,0,0] op_sel_hi:[0,1,1] neg_lo:[0,0,1] neg_hi:[0,0,1]
	v_exp_f32_e32 v112, v112
	v_exp_f32_e32 v113, v113
	v_exp_f32_e32 v114, v114
	v_exp_f32_e32 v115, v115
	v_pk_fma_f32 v[116:117], v[104:105], v[140:141], v[144:145] op_sel:[1,0,0] op_sel_hi:[1,1,1] neg_lo:[0,0,1] neg_hi:[0,0,1]
	v_pk_fma_f32 v[118:119], v[104:105], v[142:143], v[146:147] op_sel:[1,0,0] op_sel_hi:[1,1,1] neg_lo:[0,0,1] neg_hi:[0,0,1]
	v_exp_f32_e32 v116, v116
	v_exp_f32_e32 v117, v117
	v_exp_f32_e32 v118, v118
	v_exp_f32_e32 v119, v119
	v_pk_add_f32 v[152:153], v[152:153], v[112:113]
	v_pk_add_f32 v[154:155], v[154:155], v[114:115]
	v_pk_fma_f32 v[164:165], v[112:113], v[104:105], v[164:165] op_sel:[0,0,0] op_sel_hi:[1,0,1]
	v_pk_fma_f32 v[166:167], v[114:115], v[104:105], v[166:167] op_sel:[0,0,0] op_sel_hi:[1,0,1]
	v_pk_add_f32 v[152:153], v[152:153], v[116:117]
	v_pk_add_f32 v[154:155], v[154:155], v[118:119]
	v_pk_fma_f32 v[164:165], v[116:117], v[104:105], v[164:165] op_sel:[0,1,0] op_sel_hi:[1,1,1]
	v_pk_fma_f32 v[166:167], v[118:119], v[104:105], v[166:167] op_sel:[0,1,0] op_sel_hi:[1,1,1]
	v_pk_fma_f32 v[112:113], v[106:107], v[140:141], v[144:145] op_sel:[0,0,0] op_sel_hi:[0,1,1] neg_lo:[0,0,1] neg_hi:[0,0,1]
	v_pk_fma_f32 v[114:115], v[106:107], v[142:143], v[146:147] op_sel:[0,0,0] op_sel_hi:[0,1,1] neg_lo:[0,0,1] neg_hi:[0,0,1]
	v_exp_f32_e32 v112, v112
	v_exp_f32_e32 v113, v113
	v_exp_f32_e32 v114, v114
	v_exp_f32_e32 v115, v115
	v_pk_fma_f32 v[116:117], v[106:107], v[140:141], v[144:145] op_sel:[1,0,0] op_sel_hi:[1,1,1] neg_lo:[0,0,1] neg_hi:[0,0,1]
	v_pk_fma_f32 v[118:119], v[106:107], v[142:143], v[146:147] op_sel:[1,0,0] op_sel_hi:[1,1,1] neg_lo:[0,0,1] neg_hi:[0,0,1]
	v_exp_f32_e32 v116, v116
	v_exp_f32_e32 v117, v117
	v_exp_f32_e32 v118, v118
	v_exp_f32_e32 v119, v119
	v_pk_add_f32 v[152:153], v[152:153], v[112:113]
	v_pk_add_f32 v[154:155], v[154:155], v[114:115]
	v_pk_fma_f32 v[164:165], v[112:113], v[106:107], v[164:165] op_sel:[0,0,0] op_sel_hi:[1,0,1]
	v_pk_fma_f32 v[166:167], v[114:115], v[106:107], v[166:167] op_sel:[0,0,0] op_sel_hi:[1,0,1]
	v_pk_add_f32 v[152:153], v[152:153], v[116:117]
	v_pk_add_f32 v[154:155], v[154:155], v[118:119]
	v_pk_fma_f32 v[164:165], v[116:117], v[106:107], v[164:165] op_sel:[0,1,0] op_sel_hi:[1,1,1]
	v_pk_fma_f32 v[166:167], v[118:119], v[106:107], v[166:167] op_sel:[0,1,0] op_sel_hi:[1,1,1]
	v_pk_fma_f32 v[112:113], v[108:109], v[140:141], v[144:145] op_sel:[0,0,0] op_sel_hi:[0,1,1] neg_lo:[0,0,1] neg_hi:[0,0,1]
	v_pk_fma_f32 v[114:115], v[108:109], v[142:143], v[146:147] op_sel:[0,0,0] op_sel_hi:[0,1,1] neg_lo:[0,0,1] neg_hi:[0,0,1]
	v_exp_f32_e32 v112, v112
	v_exp_f32_e32 v113, v113
	v_exp_f32_e32 v114, v114
	v_exp_f32_e32 v115, v115
	v_pk_fma_f32 v[116:117], v[108:109], v[140:141], v[144:145] op_sel:[1,0,0] op_sel_hi:[1,1,1] neg_lo:[0,0,1] neg_hi:[0,0,1]
	v_pk_fma_f32 v[118:119], v[108:109], v[142:143], v[146:147] op_sel:[1,0,0] op_sel_hi:[1,1,1] neg_lo:[0,0,1] neg_hi:[0,0,1]
	v_exp_f32_e32 v116, v116
	v_exp_f32_e32 v117, v117
	v_exp_f32_e32 v118, v118
	v_exp_f32_e32 v119, v119
	v_pk_add_f32 v[152:153], v[152:153], v[112:113]
	v_pk_add_f32 v[154:155], v[154:155], v[114:115]
	v_pk_fma_f32 v[164:165], v[112:113], v[108:109], v[164:165] op_sel:[0,0,0] op_sel_hi:[1,0,1]
	v_pk_fma_f32 v[166:167], v[114:115], v[108:109], v[166:167] op_sel:[0,0,0] op_sel_hi:[1,0,1]
	v_pk_add_f32 v[152:153], v[152:153], v[116:117]
	v_pk_add_f32 v[154:155], v[154:155], v[118:119]
	v_pk_fma_f32 v[164:165], v[116:117], v[108:109], v[164:165] op_sel:[0,1,0] op_sel_hi:[1,1,1]
	v_pk_fma_f32 v[166:167], v[118:119], v[108:109], v[166:167] op_sel:[0,1,0] op_sel_hi:[1,1,1]
	v_pk_fma_f32 v[112:113], v[110:111], v[140:141], v[144:145] op_sel:[0,0,0] op_sel_hi:[0,1,1] neg_lo:[0,0,1] neg_hi:[0,0,1]
	v_pk_fma_f32 v[114:115], v[110:111], v[142:143], v[146:147] op_sel:[0,0,0] op_sel_hi:[0,1,1] neg_lo:[0,0,1] neg_hi:[0,0,1]
	v_exp_f32_e32 v112, v112
	v_exp_f32_e32 v113, v113
	v_exp_f32_e32 v114, v114
	v_exp_f32_e32 v115, v115
	v_pk_fma_f32 v[116:117], v[110:111], v[140:141], v[144:145] op_sel:[1,0,0] op_sel_hi:[1,1,1] neg_lo:[0,0,1] neg_hi:[0,0,1]
	v_pk_fma_f32 v[118:119], v[110:111], v[142:143], v[146:147] op_sel:[1,0,0] op_sel_hi:[1,1,1] neg_lo:[0,0,1] neg_hi:[0,0,1]
	v_exp_f32_e32 v116, v116
	v_exp_f32_e32 v117, v117
	v_exp_f32_e32 v118, v118
	v_exp_f32_e32 v119, v119
	v_pk_add_f32 v[152:153], v[152:153], v[112:113]
	v_pk_add_f32 v[154:155], v[154:155], v[114:115]
	v_pk_fma_f32 v[164:165], v[112:113], v[110:111], v[164:165] op_sel:[0,0,0] op_sel_hi:[1,0,1]
	v_pk_fma_f32 v[166:167], v[114:115], v[110:111], v[166:167] op_sel:[0,0,0] op_sel_hi:[1,0,1]
	v_pk_add_f32 v[152:153], v[152:153], v[116:117]
	v_pk_add_f32 v[154:155], v[154:155], v[118:119]
	v_pk_fma_f32 v[164:165], v[116:117], v[110:111], v[164:165] op_sel:[0,1,0] op_sel_hi:[1,1,1]
	v_pk_fma_f32 v[166:167], v[118:119], v[110:111], v[166:167] op_sel:[0,1,0] op_sel_hi:[1,1,1]
	v_mov_b32_e32 v73, v164
	v_mov_b32_e32 v56, v165
	v_mov_b32_e32 v48, v166
	v_mov_b32_e32 v9, v167
	s_waitcnt lgkmcnt(0)
	s_waitcnt lgkmcnt(0)
	s_waitcnt lgkmcnt(0)
	ds_read_b128 v[128:131], v99 offset:1600
	ds_read_b128 v[182:185], v99 offset:1632
	s_waitcnt lgkmcnt(0)
	v_pk_add_f32 v[186:187], v[128:129], v[44:45]
	v_mov_b32_e32 v4, v152
	v_and_b32_e32 v0, 32, v0
	v_mov_b32_e32 v44, v4
	v_mov_b32_e32 v45, v4
	s_nop 1
	v_permlane32_swap_b32_e32 v44, v45
	v_cmp_eq_u32_e32 vcc, 0, v0
	v_mov_b32_e32 v83, v73
	v_pk_add_f32 v[188:189], v[130:131], v[46:47]
	v_cndmask_b32_e32 v0, v44, v45, vcc
	v_add_f32_e32 v0, v4, v0
	v_mov_b32_e32 v4, v73
	v_rcp_f32_e32 v0, v0
	s_nop 0
	v_permlane32_swap_b32_e32 v4, v83
	v_cndmask_b32_e32 v4, v4, v83, vcc
	v_add_f32_e32 v4, v73, v4
	v_mul_f32_e32 v0, v4, v0
	ds_read_b128 v[44:47], v99 offset:576
	ds_read_b128 v[128:131], v99 offset:608
	v_mov_b32_e32 v4, v153
	s_waitcnt lgkmcnt(0)
	v_pk_fma_f32 v[186:187], v[0:1], v[44:45], v[186:187] op_sel_hi:[0,1,1]
	v_mov_b32_e32 v8, v4
	v_mov_b32_e32 v44, v4
	s_nop 1
	v_permlane32_swap_b32_e32 v8, v44
	v_cndmask_b32_e32 v8, v8, v44, vcc
	v_add_f32_e32 v4, v4, v8
	v_mov_b32_e32 v8, v56
	v_mov_b32_e32 v67, v56
	v_rcp_f32_e32 v4, v4
	s_nop 0
	v_permlane32_swap_b32_e32 v8, v67
	v_cndmask_b32_e32 v8, v8, v67, vcc
	v_add_f32_e32 v8, v56, v8
	v_mul_f32_e32 v4, v8, v4
	v_pk_fma_f32 v[188:189], v[0:1], v[46:47], v[188:189] op_sel_hi:[0,1,1]
	ds_read_b128 v[44:47], v99 offset:832
	ds_read_b128 v[120:123], v99 offset:864
	v_mov_b32_e32 v8, v154
	s_waitcnt lgkmcnt(0)
	v_pk_fma_f32 v[84:85], v[4:5], v[44:45], v[186:187] op_sel_hi:[0,1,1]
	v_mov_b32_e32 v12, v8
	v_mov_b32_e32 v44, v8
	s_nop 1
	v_permlane32_swap_b32_e32 v12, v44
	v_cndmask_b32_e32 v12, v12, v44, vcc
	v_add_f32_e32 v8, v8, v12
	v_mov_b32_e32 v12, v48
	v_mov_b32_e32 v53, v48
	v_rcp_f32_e32 v8, v8
	s_nop 0
	v_permlane32_swap_b32_e32 v12, v53
	v_cndmask_b32_e32 v12, v12, v53, vcc
	v_add_f32_e32 v12, v48, v12
	v_mul_f32_e32 v62, v12, v8
	v_pk_fma_f32 v[90:91], v[4:5], v[46:47], v[188:189] op_sel_hi:[0,1,1]
	ds_read_b128 v[44:47], v99 offset:1088
	ds_read_b128 v[76:79], v99 offset:1120
	v_pk_add_f32 v[40:41], v[182:183], v[40:41]
	v_pk_add_f32 v[42:43], v[184:185], v[42:43]
	v_pk_fma_f32 v[40:41], v[0:1], v[128:129], v[40:41] op_sel_hi:[0,1,1]
	v_pk_fma_f32 v[42:43], v[0:1], v[130:131], v[42:43] op_sel_hi:[0,1,1]
	s_waitcnt lgkmcnt(0)
	v_pk_fma_f32 v[56:57], v[62:63], v[44:45], v[84:85] op_sel_hi:[0,1,1]
	v_pk_fma_f32 v[66:67], v[62:63], v[46:47], v[90:91] op_sel_hi:[0,1,1]
	v_pk_fma_f32 v[44:45], v[4:5], v[120:121], v[40:41] op_sel_hi:[0,1,1]
	v_pk_fma_f32 v[46:47], v[4:5], v[122:123], v[42:43] op_sel_hi:[0,1,1]
	ds_read_b128 v[40:43], v99 offset:1664
	v_pk_fma_f32 v[72:73], v[62:63], v[76:77], v[44:45] op_sel_hi:[0,1,1]
	v_pk_fma_f32 v[84:85], v[62:63], v[78:79], v[46:47] op_sel_hi:[0,1,1]
	ds_read_b128 v[44:47], v99 offset:1696
	ds_read_b128 v[76:79], v99 offset:640
	s_waitcnt lgkmcnt(0)
	v_pk_add_f32 v[80:81], v[40:41], v[36:37]
	v_pk_add_f32 v[82:83], v[42:43], v[38:39]
	ds_read_b128 v[36:39], v99 offset:672
	ds_read_b128 v[40:43], v99 offset:896
	v_pk_fma_f32 v[86:87], v[0:1], v[76:77], v[80:81] op_sel_hi:[0,1,1]
	v_pk_fma_f32 v[90:91], v[0:1], v[78:79], v[82:83] op_sel_hi:[0,1,1]
	ds_read_b128 v[76:79], v99 offset:1152
	ds_read_b128 v[80:83], v99 offset:928
	s_waitcnt lgkmcnt(0)
	v_pk_fma_f32 v[86:87], v[4:5], v[40:41], v[86:87] op_sel_hi:[0,1,1]
	v_pk_fma_f32 v[90:91], v[4:5], v[42:43], v[90:91] op_sel_hi:[0,1,1]
	ds_read_b128 v[40:43], v99 offset:1184
	v_pk_add_f32 v[32:33], v[44:45], v[32:33]
	v_pk_add_f32 v[34:35], v[46:47], v[34:35]
	v_pk_fma_f32 v[32:33], v[0:1], v[36:37], v[32:33] op_sel_hi:[0,1,1]
	v_pk_fma_f32 v[34:35], v[0:1], v[38:39], v[34:35] op_sel_hi:[0,1,1]
	v_pk_fma_f32 v[36:37], v[4:5], v[80:81], v[32:33] op_sel_hi:[0,1,1]
	v_pk_fma_f32 v[38:39], v[4:5], v[82:83], v[34:35] op_sel_hi:[0,1,1]
	ds_read_b128 v[32:35], v99 offset:1728
	s_waitcnt lgkmcnt(0)
	v_pk_fma_f32 v[80:81], v[62:63], v[40:41], v[36:37] op_sel_hi:[0,1,1]
	v_pk_fma_f32 v[82:83], v[62:63], v[42:43], v[38:39] op_sel_hi:[0,1,1]
	ds_read_b128 v[36:39], v99 offset:1760
	ds_read_b128 v[40:43], v99 offset:704
	v_mov_b32_e32 v8, v155
	v_pk_add_f32 v[44:45], v[32:33], v[28:29]
	v_pk_add_f32 v[46:47], v[34:35], v[30:31]
	ds_read_b128 v[28:31], v99 offset:736
	ds_read_b128 v[32:35], v99 offset:960
	v_mov_b32_e32 v10, v8
	v_mov_b32_e32 v11, v8
	s_nop 1
	v_permlane32_swap_b32_e32 v10, v11
	v_cndmask_b32_e32 v10, v10, v11, vcc
	v_pk_fma_f32 v[76:77], v[62:63], v[76:77], v[86:87] op_sel_hi:[0,1,1]
	v_pk_fma_f32 v[78:79], v[62:63], v[78:79], v[90:91] op_sel_hi:[0,1,1]
	s_waitcnt lgkmcnt(0)
	v_pk_fma_f32 v[86:87], v[0:1], v[40:41], v[44:45] op_sel_hi:[0,1,1]
	v_pk_fma_f32 v[90:91], v[0:1], v[42:43], v[46:47] op_sel_hi:[0,1,1]
	ds_read_b128 v[40:43], v99 offset:1216
	ds_read_b128 v[44:47], v99 offset:992
	v_add_f32_e32 v8, v8, v10
	v_mov_b32_e32 v10, v9
	v_mov_b32_e32 v11, v9
	s_nop 1
	v_permlane32_swap_b32_e32 v10, v11
	v_pk_fma_f32 v[86:87], v[4:5], v[32:33], v[86:87] op_sel_hi:[0,1,1]
	v_pk_fma_f32 v[90:91], v[4:5], v[34:35], v[90:91] op_sel_hi:[0,1,1]
	ds_read_b128 v[32:35], v99 offset:1248
	v_rcp_f32_e32 v8, v8
	v_cndmask_b32_e32 v14, v10, v11, vcc
	ds_read_b128 v[10:13], v99 offset:1344
	s_waitcnt lgkmcnt(0)
	v_pk_fma_f32 v[86:87], v[62:63], v[40:41], v[86:87] op_sel_hi:[0,1,1]
	v_pk_fma_f32 v[90:91], v[62:63], v[42:43], v[90:91] op_sel_hi:[0,1,1]
	v_add_f32_e32 v9, v9, v14
	ds_read_b128 v[14:17], v99 offset:1824
	ds_read_b128 v[40:43], v99 offset:1376
	v_mul_f32_e32 v60, v9, v8
	v_pk_fma_f32 v[68:69], v[60:61], v[10:11], v[56:57] op_sel_hi:[0,1,1]
	ds_read_b128 v[8:11], v99 offset:800
	s_waitcnt lgkmcnt(0)
	v_pk_add_f32 v[26:27], v[16:17], v[26:27]
	ds_read_b128 v[16:19], v99 offset:1056
	ds_read_b128 v[48:51], v99 offset:1792
	v_pk_fma_f32 v[66:67], v[60:61], v[12:13], v[66:67] op_sel_hi:[0,1,1]
	v_pk_add_f32 v[22:23], v[14:15], v[22:23]
	ds_read_b128 v[12:15], v99 offset:768
	v_pk_fma_f32 v[26:27], v[0:1], v[10:11], v[26:27] op_sel_hi:[0,1,1]
	v_pk_fma_f32 v[22:23], v[0:1], v[8:9], v[22:23] op_sel_hi:[0,1,1]
	ds_read_b128 v[8:11], v99 offset:1024
	ds_read_b128 v[52:55], v99 offset:1312
	s_waitcnt lgkmcnt(0)
	v_pk_fma_f32 v[26:27], v[4:5], v[18:19], v[26:27] op_sel_hi:[0,1,1]
	v_pk_fma_f32 v[22:23], v[4:5], v[16:17], v[22:23] op_sel_hi:[0,1,1]
	ds_read_b128 v[16:19], v99 offset:1280
	v_pk_add_f32 v[2:3], v[48:49], v[2:3]
	v_pk_add_f32 v[20:21], v[50:51], v[20:21]
	v_pk_fma_f32 v[2:3], v[0:1], v[12:13], v[2:3] op_sel_hi:[0,1,1]
	v_pk_fma_f32 v[2:3], v[4:5], v[8:9], v[2:3] op_sel_hi:[0,1,1]
	s_waitcnt lgkmcnt(0)
	v_pk_fma_f32 v[12:13], v[62:63], v[16:17], v[2:3] op_sel_hi:[0,1,1]
	v_pk_add_f32 v[2:3], v[36:37], v[6:7]
	v_pk_add_f32 v[6:7], v[38:39], v[24:25]
	v_pk_fma_f32 v[14:15], v[0:1], v[14:15], v[20:21] op_sel_hi:[0,1,1]
	v_pk_fma_f32 v[2:3], v[0:1], v[28:29], v[2:3] op_sel_hi:[0,1,1]
	v_pk_fma_f32 v[6:7], v[0:1], v[30:31], v[6:7] op_sel_hi:[0,1,1]
	v_add_f32_e32 v0, 0, v68
	v_add_f32_e32 v0, v69, v0
	v_pk_fma_f32 v[10:11], v[4:5], v[10:11], v[14:15] op_sel_hi:[0,1,1]
	v_pk_fma_f32 v[14:15], v[4:5], v[44:45], v[2:3] op_sel_hi:[0,1,1]
	v_pk_fma_f32 v[16:17], v[4:5], v[46:47], v[6:7] op_sel_hi:[0,1,1]
	v_add_f32_e32 v0, v66, v0
	ds_read_b128 v[56:59], v99 offset:1568
	v_pk_fma_f32 v[26:27], v[62:63], v[54:55], v[26:27] op_sel_hi:[0,1,1]
	v_pk_fma_f32 v[22:23], v[62:63], v[52:53], v[22:23] op_sel_hi:[0,1,1]
	ds_read_b128 v[52:55], v99 offset:1536
	v_lshlrev_b32_e32 v100, 2, v5
	ds_read_b128 v[2:5], v99 offset:1408
	ds_read_b128 v[6:9], v99 offset:1440
	v_pk_fma_f32 v[24:25], v[62:63], v[32:33], v[14:15] op_sel_hi:[0,1,1]
	v_pk_fma_f32 v[32:33], v[62:63], v[34:35], v[16:17] op_sel_hi:[0,1,1]
	v_pk_fma_f32 v[34:35], v[60:61], v[40:41], v[72:73] op_sel_hi:[0,1,1]
	v_add_f32_e32 v0, v67, v0
	v_add_f32_e32 v0, v34, v0
	v_pk_fma_f32 v[36:37], v[60:61], v[42:43], v[84:85] op_sel_hi:[0,1,1]
	v_add_f32_e32 v0, v35, v0
	v_add_f32_e32 v0, v36, v0
	v_add_f32_e32 v0, v37, v0
	s_waitcnt lgkmcnt(0)
	v_pk_fma_f32 v[2:3], v[60:61], v[2:3], v[76:77] op_sel_hi:[0,1,1]
	v_add_f32_e32 v0, v2, v0
	v_add_f32_e32 v0, v3, v0
	v_pk_fma_f32 v[4:5], v[60:61], v[4:5], v[78:79] op_sel_hi:[0,1,1]
	v_pk_fma_f32 v[10:11], v[62:63], v[18:19], v[10:11] op_sel_hi:[0,1,1]
	v_add_f32_e32 v0, v4, v0
	v_pk_fma_f32 v[28:29], v[60:61], v[54:55], v[10:11] op_sel_hi:[0,1,1]
	v_pk_fma_f32 v[30:31], v[60:61], v[52:53], v[12:13] op_sel_hi:[0,1,1]
	ds_read_b128 v[10:13], v99 offset:1472
	ds_read_b128 v[14:17], v99 offset:1504
	v_add_f32_e32 v0, v5, v0
	v_pk_fma_f32 v[6:7], v[60:61], v[6:7], v[80:81] op_sel_hi:[0,1,1]
	v_add_f32_e32 v0, v6, v0
	v_add_f32_e32 v0, v7, v0
	v_pk_fma_f32 v[8:9], v[60:61], v[8:9], v[82:83] op_sel_hi:[0,1,1]
	v_add_f32_e32 v0, v8, v0
	v_add_f32_e32 v0, v9, v0
	s_waitcnt lgkmcnt(0)
	v_pk_fma_f32 v[10:11], v[60:61], v[10:11], v[86:87] op_sel_hi:[0,1,1]
	v_add_f32_e32 v0, v10, v0
	v_add_f32_e32 v0, v11, v0
	v_pk_fma_f32 v[12:13], v[60:61], v[12:13], v[90:91] op_sel_hi:[0,1,1]
	v_add_f32_e32 v0, v12, v0
	v_add_f32_e32 v0, v13, v0
	v_pk_fma_f32 v[14:15], v[60:61], v[14:15], v[24:25] op_sel_hi:[0,1,1]
	v_add_f32_e32 v0, v14, v0
	v_pk_fma_f32 v[16:17], v[60:61], v[16:17], v[32:33] op_sel_hi:[0,1,1]
	v_add_f32_e32 v0, v15, v0
	v_add_f32_e32 v0, v16, v0
	v_add_f32_e32 v0, v17, v0
	v_add_f32_e32 v0, v30, v0
	v_add_f32_e32 v0, v31, v0
	v_add_f32_e32 v0, v28, v0
	v_pk_fma_f32 v[22:23], v[60:61], v[56:57], v[22:23] op_sel_hi:[0,1,1]
	v_add_f32_e32 v0, v29, v0
	v_add_f32_e32 v0, v22, v0
	v_pk_fma_f32 v[26:27], v[60:61], v[58:59], v[26:27] op_sel_hi:[0,1,1]
	v_add_f32_e32 v0, v23, v0
	v_add_f32_e32 v0, v26, v0
	v_add_f32_e32 v0, v27, v0
	v_mov_b32_e32 v24, v0
	v_mov_b32_e32 v25, v0
	s_nop 1
	v_permlane32_swap_b32_e32 v24, v25
	v_cndmask_b32_e32 v24, v24, v25, vcc
	v_add_f32_e32 v0, v0, v24
	v_mul_f32_e32 v0, 0x3c800000, v0
	v_pk_add_f32 v[24:25], v[68:69], v[0:1] op_sel_hi:[1,0] neg_lo:[0,1] neg_hi:[0,1]
	v_pk_add_f32 v[38:39], v[66:67], v[0:1] op_sel_hi:[1,0] neg_lo:[0,1] neg_hi:[0,1]
	v_pk_mul_f32 v[32:33], v[24:25], v[24:25]
	v_pk_mul_f32 v[40:41], v[38:39], v[38:39]
	v_pk_add_f32 v[34:35], v[34:35], v[0:1] op_sel_hi:[1,0] neg_lo:[0,1] neg_hi:[0,1]
	v_pk_add_f32 v[36:37], v[36:37], v[0:1] op_sel_hi:[1,0] neg_lo:[0,1] neg_hi:[0,1]
	v_pk_add_f32 v[46:47], v[2:3], v[0:1] op_sel_hi:[1,0] neg_lo:[0,1] neg_hi:[0,1]
	v_pk_add_f32 v[48:49], v[4:5], v[0:1] op_sel_hi:[1,0] neg_lo:[0,1] neg_hi:[0,1]
	v_pk_add_f32 v[50:51], v[6:7], v[0:1] op_sel_hi:[1,0] neg_lo:[0,1] neg_hi:[0,1]
	v_pk_add_f32 v[52:53], v[8:9], v[0:1] op_sel_hi:[1,0] neg_lo:[0,1] neg_hi:[0,1]
	v_pk_add_f32 v[54:55], v[10:11], v[0:1] op_sel_hi:[1,0] neg_lo:[0,1] neg_hi:[0,1]
	v_pk_add_f32 v[56:57], v[12:13], v[0:1] op_sel_hi:[1,0] neg_lo:[0,1] neg_hi:[0,1]
	v_pk_add_f32 v[58:59], v[14:15], v[0:1] op_sel_hi:[1,0] neg_lo:[0,1] neg_hi:[0,1]
	v_pk_add_f32 v[60:61], v[16:17], v[0:1] op_sel_hi:[1,0] neg_lo:[0,1] neg_hi:[0,1]
	v_pk_add_f32 v[30:31], v[30:31], v[0:1] op_sel_hi:[1,0] neg_lo:[0,1] neg_hi:[0,1]
	v_pk_add_f32 v[28:29], v[28:29], v[0:1] op_sel_hi:[1,0] neg_lo:[0,1] neg_hi:[0,1]
	v_pk_add_f32 v[22:23], v[22:23], v[0:1] op_sel_hi:[1,0] neg_lo:[0,1] neg_hi:[0,1]
	v_pk_add_f32 v[26:27], v[26:27], v[0:1] op_sel_hi:[1,0] neg_lo:[0,1] neg_hi:[0,1]
	v_add_f32_e32 v0, v32, v33
	v_add_f32_e32 v0, v40, v0
	v_pk_mul_f32 v[42:43], v[34:35], v[34:35]
	v_add_f32_e32 v0, v41, v0
	v_add_f32_e32 v0, v42, v0
	v_pk_mul_f32 v[44:45], v[36:37], v[36:37]
	v_add_f32_e32 v0, v43, v0
	v_add_f32_e32 v0, v44, v0
	v_pk_mul_f32 v[2:3], v[46:47], v[46:47]
	v_add_f32_e32 v0, v45, v0
	v_add_f32_e32 v0, v2, v0
	v_pk_mul_f32 v[4:5], v[48:49], v[48:49]
	v_add_f32_e32 v0, v3, v0
	v_add_f32_e32 v0, v4, v0
	v_pk_mul_f32 v[6:7], v[50:51], v[50:51]
	v_add_f32_e32 v0, v5, v0
	v_add_f32_e32 v0, v6, v0
	v_pk_mul_f32 v[8:9], v[52:53], v[52:53]
	v_add_f32_e32 v0, v7, v0
	v_add_f32_e32 v0, v8, v0
	v_pk_mul_f32 v[10:11], v[54:55], v[54:55]
	v_add_f32_e32 v0, v9, v0
	v_add_f32_e32 v0, v10, v0
	v_pk_mul_f32 v[12:13], v[56:57], v[56:57]
	v_add_f32_e32 v0, v11, v0
	v_add_f32_e32 v0, v12, v0
	v_pk_mul_f32 v[14:15], v[58:59], v[58:59]
	v_add_f32_e32 v0, v13, v0
	v_add_f32_e32 v0, v14, v0
	v_pk_mul_f32 v[16:17], v[60:61], v[60:61]
	v_add_f32_e32 v0, v15, v0
	v_add_f32_e32 v0, v16, v0
	v_pk_mul_f32 v[32:33], v[30:31], v[30:31]
	v_add_f32_e32 v0, v17, v0
	v_add_f32_e32 v0, v32, v0
	v_pk_mul_f32 v[2:3], v[28:29], v[28:29]
	v_add_f32_e32 v0, v33, v0
	v_add_f32_e32 v0, v2, v0
	v_pk_mul_f32 v[4:5], v[22:23], v[22:23]
	v_add_f32_e32 v0, v3, v0
	v_add_f32_e32 v0, v4, v0
	v_pk_mul_f32 v[6:7], v[26:27], v[26:27]
	v_add_f32_e32 v0, v5, v0
	v_add_f32_e32 v0, v6, v0
	v_add_f32_e32 v0, v7, v0
	v_mov_b32_e32 v2, v0
	v_mov_b32_e32 v3, v0
	s_nop 1
	v_permlane32_swap_b32_e32 v2, v3
	v_cndmask_b32_e32 v2, v2, v3, vcc
	v_add_f32_e32 v0, v0, v2
	v_mov_b32_e32 v2, 0x3727c5ac
	v_fmac_f32_e32 v2, 0x3c800000, v0
	ds_read_b128 v[18:21], v99 offset:3392
	v_rsq_f32_e32 v0, v2
	ds_read_b128 v[2:5], v99 offset:3136
	ds_read_b128 v[6:9], v99 offset:3168
	ds_read_b128 v[10:13], v99 offset:3424
	ds_read_b128 v[14:17], v99 offset:3456
	s_load_dwordx2 s[0:1], s[0:1], 0x40
	v_lshlrev_b32_e32 v101, 4, v1
	v_pk_mul_f32 v[24:25], v[24:25], v[0:1] op_sel_hi:[1,0]
	s_mov_b32 s2, 8
	s_waitcnt lgkmcnt(0)
	v_pk_fma_f32 v[86:87], v[2:3], v[24:25], v[18:19]
	v_pk_mul_f32 v[2:3], v[38:39], v[0:1] op_sel_hi:[1,0]
	v_pk_mul_f32 v[24:25], v[34:35], v[0:1] op_sel_hi:[1,0]
	v_pk_fma_f32 v[84:85], v[4:5], v[2:3], v[20:21]
	ds_read_b128 v[2:5], v99 offset:3200
	ds_read_b128 v[18:21], v99 offset:3232
	v_pk_fma_f32 v[82:83], v[6:7], v[24:25], v[10:11]
	v_pk_mul_f32 v[6:7], v[36:37], v[0:1] op_sel_hi:[1,0]
	v_pk_mul_f32 v[24:25], v[46:47], v[0:1] op_sel_hi:[1,0]
	v_pk_fma_f32 v[80:81], v[8:9], v[6:7], v[12:13]
	ds_read_b128 v[6:9], v99 offset:3488
	ds_read_b128 v[10:13], v99 offset:3520
	s_waitcnt lgkmcnt(0)
	v_pk_fma_f32 v[78:79], v[2:3], v[24:25], v[14:15]
	v_pk_mul_f32 v[2:3], v[48:49], v[0:1] op_sel_hi:[1,0]
	v_pk_mul_f32 v[24:25], v[50:51], v[0:1] op_sel_hi:[1,0]
	v_pk_fma_f32 v[76:77], v[4:5], v[2:3], v[16:17]
	ds_read_b128 v[2:5], v99 offset:3264
	ds_read_b128 v[14:17], v99 offset:3296
	v_pk_fma_f32 v[74:75], v[18:19], v[24:25], v[6:7]
	v_pk_mul_f32 v[6:7], v[52:53], v[0:1] op_sel_hi:[1,0]
	v_pk_mul_f32 v[24:25], v[54:55], v[0:1] op_sel_hi:[1,0]
	v_pk_fma_f32 v[72:73], v[20:21], v[6:7], v[8:9]
	ds_read_b128 v[6:9], v99 offset:3552
	ds_read_b128 v[18:21], v99 offset:3584
	s_waitcnt lgkmcnt(0)
	v_pk_fma_f32 v[70:71], v[2:3], v[24:25], v[10:11]
	v_pk_mul_f32 v[2:3], v[56:57], v[0:1] op_sel_hi:[1,0]
	v_pk_mul_f32 v[24:25], v[58:59], v[0:1] op_sel_hi:[1,0]
	v_pk_fma_f32 v[68:69], v[4:5], v[2:3], v[12:13]
	ds_read_b128 v[2:5], v99 offset:3328
	ds_read_b128 v[10:13], v99 offset:3360
	v_pk_fma_f32 v[66:67], v[14:15], v[24:25], v[6:7]
	v_pk_mul_f32 v[6:7], v[60:61], v[0:1] op_sel_hi:[1,0]
	v_pk_mul_f32 v[14:15], v[30:31], v[0:1] op_sel_hi:[1,0]
	v_pk_fma_f32 v[96:97], v[16:17], v[6:7], v[8:9]
	ds_read_b128 v[6:9], v99 offset:3616
	s_waitcnt lgkmcnt(0)
	v_pk_fma_f32 v[88:89], v[2:3], v[14:15], v[18:19]
	v_pk_mul_f32 v[2:3], v[28:29], v[0:1] op_sel_hi:[1,0]
	s_waitcnt vmcnt(0)
	v_cvt_pkrtz_f16_f32 v48, v86, v87
	v_pk_fma_f32 v[90:91], v[4:5], v[2:3], v[20:21]
	v_pk_mul_f32 v[2:3], v[22:23], v[0:1] op_sel_hi:[1,0]
	v_cvt_pkrtz_f16_f32 v49, v84, v85
	v_pk_fma_f32 v[92:93], v[10:11], v[2:3], v[6:7]
	v_pk_mul_f32 v[2:3], v[26:27], v[0:1] op_sel_hi:[1,0]
	v_mov_b32_e32 v0, 0
	v_pk_fma_f32 v[94:95], v[12:13], v[2:3], v[8:9]
	v_cvt_pkrtz_f16_f32 v50, v82, v83
	v_cvt_pkrtz_f16_f32 v51, v80, v81
	v_cvt_pkrtz_f16_f32 v52, v78, v79
	v_cvt_pkrtz_f16_f32 v53, v76, v77
	v_cvt_pkrtz_f16_f32 v54, v74, v75
	v_cvt_pkrtz_f16_f32 v55, v72, v73
	v_cvt_pkrtz_f16_f32 v56, v70, v71
	v_cvt_pkrtz_f16_f32 v57, v68, v69
	v_cvt_pkrtz_f16_f32 v58, v66, v67
	v_cvt_pkrtz_f16_f32 v59, v96, v97
	v_cvt_pkrtz_f16_f32 v60, v88, v89
	v_cvt_pkrtz_f16_f32 v61, v90, v91
	v_cvt_pkrtz_f16_f32 v62, v92, v93
	v_cvt_pkrtz_f16_f32 v63, v94, v95
	v_mov_b32_e32 v1, v0
	v_mov_b32_e32 v2, v0
	v_mov_b32_e32 v3, v0
	v_mov_b32_e32 v4, v0
	v_mov_b32_e32 v5, v0
	v_mov_b32_e32 v6, v0
	v_mov_b32_e32 v7, v0
	v_mov_b32_e32 v8, v0
	v_mov_b32_e32 v9, v0
	v_mov_b32_e32 v10, v0
	v_mov_b32_e32 v11, v0
	v_mov_b32_e32 v12, v0
	v_mov_b32_e32 v13, v0
	v_mov_b32_e32 v14, v0
	v_mov_b32_e32 v15, v0
	v_mov_b32_e32 v16, v0
	v_mov_b32_e32 v17, v0
	v_mov_b32_e32 v18, v0
	v_mov_b32_e32 v19, v0
	v_mov_b32_e32 v20, v0
	v_mov_b32_e32 v21, v0
	v_mov_b32_e32 v22, v0
	v_mov_b32_e32 v23, v0
	v_mov_b32_e32 v24, v0
	v_mov_b32_e32 v25, v0
	v_mov_b32_e32 v26, v0
	v_mov_b32_e32 v27, v0
	v_mov_b32_e32 v28, v0
	v_mov_b32_e32 v29, v0
	v_mov_b32_e32 v30, v0
	v_mov_b32_e32 v31, v0
	v_or_b32_e32 v102, 0x8000, v101
	s_waitcnt vmcnt(0)
	s_barrier

	.amdhsa_kernel _Z11k1_temporalPKfS0_S0_PKDF16_S0_S0_S0_S0_Pf
		.amdhsa_group_segment_fixed_size 0
		.amdhsa_private_segment_fixed_size 0
		.amdhsa_kernarg_size 72
		.amdhsa_user_sgpr_count 2
		.amdhsa_user_sgpr_dispatch_ptr 0
		.amdhsa_user_sgpr_queue_ptr 0
		.amdhsa_user_sgpr_kernarg_segment_ptr 1
		.amdhsa_user_sgpr_dispatch_id 0
		.amdhsa_user_sgpr_kernarg_preload_length 0
		.amdhsa_user_sgpr_kernarg_preload_offset 0
		.amdhsa_user_sgpr_private_segment_size 0
		.amdhsa_uses_dynamic_stack 0
		.amdhsa_enable_private_segment 0
		.amdhsa_system_sgpr_workgroup_id_x 1
		.amdhsa_system_sgpr_workgroup_id_y 0
		.amdhsa_system_sgpr_workgroup_id_z 0
		.amdhsa_system_sgpr_workgroup_info 0
		.amdhsa_system_vgpr_workitem_id 0
		.amdhsa_next_free_vgpr 247
		.amdhsa_next_free_sgpr 34
		.amdhsa_accum_offset 248
		.amdhsa_reserve_vcc 1
		.amdhsa_float_round_mode_32 0
		.amdhsa_float_round_mode_16_64 0
		.amdhsa_float_denorm_mode_32 3
		.amdhsa_float_denorm_mode_16_64 3
		.amdhsa_dx10_clamp 1
		.amdhsa_ieee_mode 1
		.amdhsa_fp16_overflow 0
		.amdhsa_tg_split 0
		.amdhsa_exception_fp_ieee_invalid_op 0
		.amdhsa_exception_fp_denorm_src 0
		.amdhsa_exception_fp_ieee_div_zero 0
		.amdhsa_exception_fp_ieee_overflow 0
		.amdhsa_exception_fp_ieee_underflow 0
		.amdhsa_exception_fp_ieee_inexact 0
		.amdhsa_exception_int_div_zero 0
	.end_amdhsa_kernel

amdhsa.kernels:
  - .agpr_count:     0
    .args:
      - .offset:         0
        .size:           272
        .value_kind:     by_value
    .group_segment_fixed_size: 27780
    .kernarg_segment_align: 8
    .kernarg_segment_size: 272
    .language:       OpenCL C
    .language_version:
      - 2
      - 0
    .max_flat_workgroup_size: 1024
    .name:           _Z6k_prep5PrepP
    .private_segment_fixed_size: 0
    .sgpr_count:     106
    .sgpr_spill_count: 0
    .symbol:         _Z6k_prep5PrepP.kd
    .uniform_work_group_size: 1
    .uses_dynamic_stack: false
    .vgpr_count:     135
    .vgpr_spill_count: 0
    .wavefront_size: 64
  - .agpr_count:     0
    .args:
      - .actual_access:  read_only
        .address_space:  global
        .offset:         0
        .size:           8
        .value_kind:     global_buffer
      - .actual_access:  read_only
        .address_space:  global
        .offset:         8
        .size:           8
        .value_kind:     global_buffer
      - .actual_access:  read_only
        .address_space:  global
        .offset:         16
        .size:           8
        .value_kind:     global_buffer
      - .address_space:  global
        .offset:         24
        .size:           8
        .value_kind:     global_buffer
      - .actual_access:  read_only
        .address_space:  global
        .offset:         32
        .size:           8
        .value_kind:     global_buffer
      - .actual_access:  read_only
        .address_space:  global
        .offset:         40
        .size:           8
        .value_kind:     global_buffer
      - .actual_access:  read_only
        .address_space:  global
        .offset:         48
        .size:           8
        .value_kind:     global_buffer
      - .actual_access:  read_only
        .address_space:  global
        .offset:         56
        .size:           8
        .value_kind:     global_buffer
      - .actual_access:  write_only
        .address_space:  global
        .offset:         64
        .size:           8
        .value_kind:     global_buffer
    .group_segment_fixed_size: 0
    .kernarg_segment_align: 8
    .kernarg_segment_size: 72
    .language:       OpenCL C
    .language_version:
      - 2
      - 0
    .max_flat_workgroup_size: 384
    .name:           _Z11k1_temporalPKfS0_S0_PKDF16_S0_S0_S0_S0_Pf
    .private_segment_fixed_size: 0
    .sgpr_count:     40
    .sgpr_spill_count: 0
    .symbol:         _Z11k1_temporalPKfS0_S0_PKDF16_S0_S0_S0_S0_Pf.kd
    .uniform_work_group_size: 1
    .uses_dynamic_stack: false
    .vgpr_count:     247
    .vgpr_spill_count: 0
    .wavefront_size: 64
  - .agpr_count:     0
    .args:
      - .address_space:  global
        .offset:         0
        .size:           8
        .value_kind:     global_buffer
      - .address_space:  global
        .offset:         8
        .size:           8
        .value_kind:     global_buffer
      - .actual_access:  read_only
        .address_space:  global
        .offset:         16
        .size:           8
        .value_kind:     global_buffer
      - .actual_access:  read_only
        .address_space:  global
        .offset:         24
        .size:           8
        .value_kind:     global_buffer
      - .actual_access:  read_only
        .address_space:  global
        .offset:         32
        .size:           8
        .value_kind:     global_buffer
      - .actual_access:  read_only
        .address_space:  global
        .offset:         40
        .size:           8
        .value_kind:     global_buffer
      - .actual_access:  read_only
        .address_space:  global
        .offset:         48
        .size:           8
        .value_kind:     global_buffer
      - .actual_access:  read_only
        .address_space:  global
        .offset:         56
        .size:           8
        .value_kind:     global_buffer
      - .actual_access:  read_only
        .address_space:  global
        .offset:         64
        .size:           8
        .value_kind:     global_buffer
      - .actual_access:  read_only
        .address_space:  global
        .offset:         72
        .size:           8
        .value_kind:     global_buffer
      - .actual_access:  read_only
        .address_space:  global
        .offset:         80
        .size:           8
        .value_kind:     global_buffer
      - .actual_access:  read_only
        .address_space:  global
        .offset:         88
        .size:           8
        .value_kind:     global_buffer
      - .actual_access:  read_only
        .address_space:  global
        .offset:         96
        .size:           8
        .value_kind:     global_buffer
      - .actual_access:  read_only
        .address_space:  global
        .offset:         104
        .size:           8
        .value_kind:     global_buffer
      - .actual_access:  read_only
        .address_space:  global
        .offset:         112
        .size:           8
        .value_kind:     global_buffer
      - .actual_access:  read_only
        .address_space:  global
        .offset:         120
        .size:           8
        .value_kind:     global_buffer
      - .address_space:  global
        .offset:         128
        .size:           8
        .value_kind:     global_buffer
      - .actual_access:  write_only
        .address_space:  global
        .offset:         136
        .size:           8
        .value_kind:     global_buffer
      - .actual_access:  write_only
        .address_space:  global
        .offset:         144
        .size:           8
        .value_kind:     global_buffer
      - .actual_access:  write_only
        .address_space:  global
        .offset:         152
        .size:           8
        .value_kind:     global_buffer
      - .actual_access:  write_only
        .address_space:  global
        .offset:         160
        .size:           8
        .value_kind:     global_buffer
    .group_segment_fixed_size: 0
    .kernarg_segment_align: 8
    .kernarg_segment_size: 168
    .language:       OpenCL C
    .language_version:
      - 2
      - 0
    .max_flat_workgroup_size: 512
    .name:           _Z10k2_featurePKfPKDF16_S0_S0_S0_S0_S0_S0_PKyS0_S0_S0_S0_S0_S0_S0_PfS5_S5_S5_S5_
    .private_segment_fixed_size: 0
    .sgpr_count:     38
    .sgpr_spill_count: 0
    .symbol:         _Z10k2_featurePKfPKDF16_S0_S0_S0_S0_S0_S0_PKyS0_S0_S0_S0_S0_S0_S0_PfS5_S5_S5_S5_.kd
    .uniform_work_group_size: 1
    .uses_dynamic_stack: false
    .vgpr_count:     256
    .vgpr_spill_count: 0
    .wavefront_size: 64
  - .agpr_count:     0
    .args:
      - .actual_access:  read_only
        .address_space:  global
        .offset:         0
        .size:           8
        .value_kind:     global_buffer
      - .actual_access:  read_only
        .address_space:  global
        .offset:         8
        .size:           8
        .value_kind:     global_buffer
      - .actual_access:  read_only
        .address_space:  global
        .offset:         16
        .size:           8
        .value_kind:     global_buffer
      - .actual_access:  read_only
        .address_space:  global
        .offset:         24
        .size:           8
        .value_kind:     global_buffer
      - .actual_access:  read_only
        .address_space:  global
        .offset:         32
        .size:           8
        .value_kind:     global_buffer
      - .actual_access:  write_only
        .address_space:  global
        .offset:         40
        .size:           8
        .value_kind:     global_buffer
      - .actual_access:  write_only
        .address_space:  global
        .offset:         48
        .size:           8
        .value_kind:     global_buffer
      - .address_space:  global
        .offset:         56
        .size:           8
        .value_kind:     global_buffer
      - .actual_access:  write_only
        .address_space:  global
        .offset:         64
        .size:           8
        .value_kind:     global_buffer
    .group_segment_fixed_size: 56768
    .kernarg_segment_align: 8
    .kernarg_segment_size: 72
    .language:       OpenCL C
    .language_version:
      - 2
      - 0
    .max_flat_workgroup_size: 768
    .name:           _Z5k3_vqPKDF16_S0_S0_S0_PKfPiPfS3_S4_
    .private_segment_fixed_size: 0
    .sgpr_count:     54
    .sgpr_spill_count: 0
    .symbol:         _Z5k3_vqPKDF16_S0_S0_S0_PKfPiPfS3_S4_.kd
    .uniform_work_group_size: 1
    .uses_dynamic_stack: false
    .vgpr_count:     88
    .vgpr_spill_count: 0
    .wavefront_size: 64
  - .agpr_count:     0
    .args:
      - .actual_access:  read_only
        .address_space:  global
        .offset:         0
        .size:           8
        .value_kind:     global_buffer
      - .actual_access:  read_only
        .address_space:  global
        .offset:         8
        .size:           8
        .value_kind:     global_buffer
      - .address_space:  global
        .offset:         16
        .size:           8
        .value_kind:     global_buffer
      - .actual_access:  read_only
        .address_space:  global
        .offset:         24
        .size:           8
        .value_kind:     global_buffer
      - .actual_access:  read_only
        .address_space:  global
        .offset:         32
        .size:           8
        .value_kind:     global_buffer
      - .actual_access:  read_only
        .address_space:  global
        .offset:         40
        .size:           8
        .value_kind:     global_buffer
      - .actual_access:  read_only
        .address_space:  global
        .offset:         48
        .size:           8
        .value_kind:     global_buffer
      - .actual_access:  read_only
        .address_space:  global
        .offset:         56
        .size:           8
        .value_kind:     global_buffer
      - .actual_access:  read_only
        .address_space:  global
        .offset:         64
        .size:           8
        .value_kind:     global_buffer
      - .actual_access:  read_only
        .address_space:  global
        .offset:         72
        .size:           8
        .value_kind:     global_buffer
      - .actual_access:  read_only
        .address_space:  global
        .offset:         80
        .size:           8
        .value_kind:     global_buffer
      - .address_space:  global
        .offset:         88
        .size:           8
        .value_kind:     global_buffer
      - .actual_access:  read_only
        .address_space:  global
        .offset:         96
        .size:           8
        .value_kind:     global_buffer
      - .actual_access:  read_only
        .address_space:  global
        .offset:         104
        .size:           8
        .value_kind:     global_buffer
      - .actual_access:  read_only
        .address_space:  global
        .offset:         112
        .size:           8
        .value_kind:     global_buffer
      - .actual_access:  read_only
        .address_space:  global
        .offset:         120
        .size:           8
        .value_kind:     global_buffer
      - .actual_access:  read_only
        .address_space:  global
        .offset:         128
        .size:           8
        .value_kind:     global_buffer
      - .address_space:  global
        .offset:         136
        .size:           8
        .value_kind:     global_buffer
      - .address_space:  global
        .offset:         144
        .size:           8
        .value_kind:     global_buffer
      - .actual_access:  write_only
        .address_space:  global
        .offset:         152
        .size:           8
        .value_kind:     global_buffer
      - .offset:         160
        .size:           4
        .value_kind:     hidden_block_count_x
      - .offset:         164
        .size:           4
        .value_kind:     hidden_block_count_y
      - .offset:         168
        .size:           4
        .value_kind:     hidden_block_count_z
      - .offset:         172
        .size:           2
        .value_kind:     hidden_group_size_x
      - .offset:         174
        .size:           2
        .value_kind:     hidden_group_size_y
      - .offset:         176
        .size:           2
        .value_kind:     hidden_group_size_z
      - .offset:         178
        .size:           2
        .value_kind:     hidden_remainder_x
      - .offset:         180
        .size:           2
        .value_kind:     hidden_remainder_y
      - .offset:         182
        .size:           2
        .value_kind:     hidden_remainder_z
      - .offset:         200
        .size:           8
        .value_kind:     hidden_global_offset_x
      - .offset:         208
        .size:           8
        .value_kind:     hidden_global_offset_y
      - .offset:         216
        .size:           8
        .value_kind:     hidden_global_offset_z
      - .offset:         224
        .size:           2
        .value_kind:     hidden_grid_dims
      - .offset:         280
        .size:           4
        .value_kind:     hidden_dynamic_lds_size
    .group_segment_fixed_size: 0
    .kernarg_segment_align: 8
    .kernarg_segment_size: 416
    .language:       OpenCL C
    .language_version:
      - 2
      - 0
    .max_flat_workgroup_size: 768
    .name:           _Z7k5_convPKDF16_PKiS0_PKfS4_S4_S4_S4_S4_S4_S4_PfS4_S4_S2_S2_S4_PiS5_S5_
    .private_segment_fixed_size: 0
    .sgpr_count:     54
    .sgpr_spill_count: 0
    .symbol:         _Z7k5_convPKDF16_PKiS0_PKfS4_S4_S4_S4_S4_S4_S4_PfS4_S4_S2_S2_S4_PiS5_S5_.kd
    .uniform_work_group_size: 1
    .uses_dynamic_stack: false
    .vgpr_count:     88
    .vgpr_spill_count: 0
    .wavefront_size: 64
